# speedup vs baseline: 1.0050x; 1.0050x over previous
.LBB1_1:
	ds_read_b128 v[212:215], v242 offset:0
	ds_read_b128 v[216:219], v242 offset:0x800
	ds_read_b128 v[220:223], v242 offset:0x1000
	ds_read_b128 v[224:227], v242 offset:0x1800
	ds_read_b128 v[228:231], v211 offset:0
	ds_read_b128 v[232:235], v211 offset:0x800
	ds_read_b128 v[236:239], v211 offset:0x1000
	s_waitcnt lgkmcnt(2)
	v_mfma_f32_16x16x32_bf16 v[174:177], v[212:215], v[228:231], v[174:177]
	v_mfma_f32_16x16x32_bf16 v[170:173], v[216:219], v[228:231], v[170:173]
	v_mfma_f32_16x16x32_bf16 v[166:169], v[220:223], v[228:231], v[166:169]
	v_mfma_f32_16x16x32_bf16 v[162:165], v[224:227], v[228:231], v[162:165]
	ds_read_b128 v[228:231], v211 offset:0x1800
	s_waitcnt lgkmcnt(2)
	v_mfma_f32_16x16x32_bf16 v[158:161], v[212:215], v[232:235], v[158:161]
	v_mfma_f32_16x16x32_bf16 v[154:157], v[216:219], v[232:235], v[154:157]
	v_mfma_f32_16x16x32_bf16 v[150:153], v[220:223], v[232:235], v[150:153]
	v_mfma_f32_16x16x32_bf16 v[146:149], v[224:227], v[232:235], v[146:149]
	ds_read_b128 v[232:235], v211 offset:0x2000
	s_waitcnt lgkmcnt(2)
	v_mfma_f32_16x16x32_bf16 v[142:145], v[212:215], v[236:239], v[142:145]
	v_mfma_f32_16x16x32_bf16 v[138:141], v[216:219], v[236:239], v[138:141]
	v_mfma_f32_16x16x32_bf16 v[134:137], v[220:223], v[236:239], v[134:137]
	v_mfma_f32_16x16x32_bf16 v[130:133], v[224:227], v[236:239], v[130:133]
	ds_read_b128 v[236:239], v211 offset:0x2800
	s_waitcnt lgkmcnt(2)
	v_mfma_f32_16x16x32_bf16 v[126:129], v[212:215], v[228:231], v[126:129]
	v_mfma_f32_16x16x32_bf16 v[122:125], v[216:219], v[228:231], v[122:125]
	v_mfma_f32_16x16x32_bf16 v[118:121], v[220:223], v[228:231], v[118:121]
	v_mfma_f32_16x16x32_bf16 v[114:117], v[224:227], v[228:231], v[114:117]
	ds_read_b128 v[228:231], v211 offset:0x3000
	s_waitcnt lgkmcnt(2)
	v_mfma_f32_16x16x32_bf16 v[110:113], v[212:215], v[232:235], v[110:113]
	v_mfma_f32_16x16x32_bf16 v[106:109], v[216:219], v[232:235], v[106:109]
	v_mfma_f32_16x16x32_bf16 v[102:105], v[220:223], v[232:235], v[102:105]
	v_mfma_f32_16x16x32_bf16 v[98:101], v[224:227], v[232:235], v[98:101]
	ds_read_b128 v[232:235], v211 offset:0x3800
	s_waitcnt lgkmcnt(2)
	v_mfma_f32_16x16x32_bf16 v[94:97], v[212:215], v[236:239], v[94:97]
	v_mfma_f32_16x16x32_bf16 v[90:93], v[216:219], v[236:239], v[90:93]
	v_mfma_f32_16x16x32_bf16 v[86:89], v[220:223], v[236:239], v[86:89]
	v_mfma_f32_16x16x32_bf16 v[82:85], v[224:227], v[236:239], v[82:85]
	s_waitcnt lgkmcnt(0)
	v_mfma_f32_16x16x32_bf16 v[78:81], v[212:215], v[228:231], v[78:81]
	v_mfma_f32_16x16x32_bf16 v[74:77], v[216:219], v[228:231], v[74:77]
	v_mfma_f32_16x16x32_bf16 v[70:73], v[220:223], v[228:231], v[70:73]
	v_mfma_f32_16x16x32_bf16 v[66:69], v[224:227], v[228:231], v[66:69]
	v_mfma_f32_16x16x32_bf16 v[62:65], v[212:215], v[232:235], v[62:65]
	v_mfma_f32_16x16x32_bf16 v[58:61], v[216:219], v[232:235], v[58:61]
	v_mfma_f32_16x16x32_bf16 v[54:57], v[220:223], v[232:235], v[54:57]
	v_mfma_f32_16x16x32_bf16 v[50:53], v[224:227], v[232:235], v[50:53]
	s_xor_b32 s0, s0, 0x10000
	s_and_b32 s1, s22, 0x3c0
	s_add_i32 s23, s0, 0
	s_lshl_b32 s0, s1, 2
	s_add_u32 s20, s25, s0
	s_waitcnt vmcnt(10)
	v_cvt_pk_bf16_f32 v46, v46, v47
	v_cvt_pk_bf16_f32 v47, v48, v49
	v_cvt_pk_bf16_f32 v48, v42, v43
	v_cvt_pk_bf16_f32 v49, v44, v45
	s_waitcnt vmcnt(8)
	v_cvt_pk_bf16_f32 v38, v38, v39
	v_cvt_pk_bf16_f32 v39, v40, v41
	v_cvt_pk_bf16_f32 v40, v34, v35
	v_add_u32_e32 v34, s23, v208
	s_addc_u32 s21, s26, 0
	s_lshl_b32 s0, s1, 1
	v_cvt_pk_bf16_f32 v41, v36, v37
	v_lshlrev_b32_e32 v182, 2, v178
	v_add_u32_e32 v35, s23, v205
	v_add_u32_e32 v36, s23, v206
	v_add_u32_e32 v37, s23, v207
	ds_write_b128 v34, v[46:49]
	ds_write_b128 v35, v[38:41]
	s_waitcnt vmcnt(7)
	ds_write_b128 v36, v[30:33] offset:32768
	s_waitcnt vmcnt(6)
	ds_write_b128 v37, v[26:29] offset:32768
	v_lshl_add_u64 v[26:27], s[20:21], 0, v[180:181]
	v_lshl_add_u64 v[28:29], s[20:21], 0, v[184:185]
	s_add_u32 s0, s27, s0
	v_lshl_add_u64 v[26:27], v[26:27], 0, v[182:183]
	v_lshl_add_u64 v[28:29], v[28:29], 0, v[182:183]
	s_addc_u32 s1, s28, 0
	v_lshlrev_b32_e32 v240, 1, v178
	v_mov_b32_e32 v241, v183
	global_load_dwordx4 v[42:45], v[26:27], off offset:16
	global_load_dwordx4 v[46:49], v[26:27], off
	global_load_dwordx4 v[34:37], v[28:29], off offset:16
	global_load_dwordx4 v[38:41], v[28:29], off
	v_lshl_add_u64 v[26:27], s[0:1], 0, v[186:187]
	v_lshl_add_u64 v[28:29], s[0:1], 0, v[188:189]
	v_lshl_add_u64 v[26:27], v[26:27], 0, v[240:241]
	v_lshl_add_u64 v[28:29], v[28:29], 0, v[240:241]
	global_load_dwordx4 v[30:33], v[26:27], off
	s_nop 0
	global_load_dwordx4 v[26:29], v[28:29], off
	ds_read_b128 v[212:215], v242 offset:0x400
	ds_read_b128 v[216:219], v242 offset:0xc00
	ds_read_b128 v[220:223], v242 offset:0x1400
	ds_read_b128 v[224:227], v242 offset:0x1c00
	ds_read_b128 v[228:231], v211 offset:0x400
	ds_read_b128 v[232:235], v211 offset:0xc00
	ds_read_b128 v[236:239], v211 offset:0x1400
	s_waitcnt lgkmcnt(2)
	v_mfma_f32_16x16x32_bf16 v[174:177], v[212:215], v[228:231], v[174:177]
	v_mfma_f32_16x16x32_bf16 v[170:173], v[216:219], v[228:231], v[170:173]
	v_mfma_f32_16x16x32_bf16 v[166:169], v[220:223], v[228:231], v[166:169]
	v_mfma_f32_16x16x32_bf16 v[162:165], v[224:227], v[228:231], v[162:165]
	ds_read_b128 v[228:231], v211 offset:0x1c00
	s_waitcnt lgkmcnt(2)
	v_mfma_f32_16x16x32_bf16 v[158:161], v[212:215], v[232:235], v[158:161]
	v_mfma_f32_16x16x32_bf16 v[154:157], v[216:219], v[232:235], v[154:157]
	v_mfma_f32_16x16x32_bf16 v[150:153], v[220:223], v[232:235], v[150:153]
	v_mfma_f32_16x16x32_bf16 v[146:149], v[224:227], v[232:235], v[146:149]
	ds_read_b128 v[232:235], v211 offset:0x2400
	s_waitcnt lgkmcnt(2)
	v_mfma_f32_16x16x32_bf16 v[142:145], v[212:215], v[236:239], v[142:145]
	v_mfma_f32_16x16x32_bf16 v[138:141], v[216:219], v[236:239], v[138:141]
	v_mfma_f32_16x16x32_bf16 v[134:137], v[220:223], v[236:239], v[134:137]
	v_mfma_f32_16x16x32_bf16 v[130:133], v[224:227], v[236:239], v[130:133]
	ds_read_b128 v[236:239], v211 offset:0x2c00
	s_waitcnt lgkmcnt(2)
	v_mfma_f32_16x16x32_bf16 v[126:129], v[212:215], v[228:231], v[126:129]
	v_mfma_f32_16x16x32_bf16 v[122:125], v[216:219], v[228:231], v[122:125]
	v_mfma_f32_16x16x32_bf16 v[118:121], v[220:223], v[228:231], v[118:121]
	v_mfma_f32_16x16x32_bf16 v[114:117], v[224:227], v[228:231], v[114:117]
	ds_read_b128 v[228:231], v211 offset:0x3400
	s_waitcnt lgkmcnt(2)
	v_mfma_f32_16x16x32_bf16 v[110:113], v[212:215], v[232:235], v[110:113]
	v_mfma_f32_16x16x32_bf16 v[106:109], v[216:219], v[232:235], v[106:109]
	v_mfma_f32_16x16x32_bf16 v[102:105], v[220:223], v[232:235], v[102:105]
	v_mfma_f32_16x16x32_bf16 v[98:101], v[224:227], v[232:235], v[98:101]
	ds_read_b128 v[232:235], v211 offset:0x3c00
	s_waitcnt lgkmcnt(2)
	v_mfma_f32_16x16x32_bf16 v[94:97], v[212:215], v[236:239], v[94:97]
	v_mfma_f32_16x16x32_bf16 v[90:93], v[216:219], v[236:239], v[90:93]
	v_mfma_f32_16x16x32_bf16 v[86:89], v[220:223], v[236:239], v[86:89]
	v_mfma_f32_16x16x32_bf16 v[82:85], v[224:227], v[236:239], v[82:85]
	s_waitcnt lgkmcnt(0)
	v_mfma_f32_16x16x32_bf16 v[78:81], v[212:215], v[228:231], v[78:81]
	v_mfma_f32_16x16x32_bf16 v[74:77], v[216:219], v[228:231], v[74:77]
	v_mfma_f32_16x16x32_bf16 v[70:73], v[220:223], v[228:231], v[70:73]
	v_mfma_f32_16x16x32_bf16 v[66:69], v[224:227], v[228:231], v[66:69]
	v_mfma_f32_16x16x32_bf16 v[62:65], v[212:215], v[232:235], v[62:65]
	v_mfma_f32_16x16x32_bf16 v[58:61], v[216:219], v[232:235], v[58:61]
	v_mfma_f32_16x16x32_bf16 v[54:57], v[220:223], v[232:235], v[54:57]
	v_mfma_f32_16x16x32_bf16 v[50:53], v[224:227], v[232:235], v[50:53]
	s_waitcnt vmcnt(10)
	v_cvt_pk_bf16_f32 v22, v22, v23
	v_cvt_pk_bf16_f32 v23, v24, v25
	v_cvt_pk_bf16_f32 v24, v6, v7
	v_cvt_pk_bf16_f32 v25, v8, v9
	v_add_u32_e32 v6, s23, v204
	s_waitcnt vmcnt(9)
	v_cvt_pk_bf16_f32 v8, v2, v3
	v_add_u32_e32 v2, s23, v201
	ds_write_b128 v6, v[22:25]
	s_waitcnt vmcnt(8)
	v_cvt_pk_bf16_f32 v6, v10, v11
	v_cvt_pk_bf16_f32 v7, v12, v13
	v_cvt_pk_bf16_f32 v9, v4, v5
	ds_write_b128 v2, v[6:9]
	v_add_u32_e32 v2, s23, v202
	s_waitcnt vmcnt(7)
	ds_write_b128 v2, v[18:21] offset:32768
	v_add_u32_e32 v2, s23, v203
	s_waitcnt vmcnt(6)
	ds_write_b128 v2, v[14:17] offset:32768
	v_lshl_add_u64 v[2:3], s[20:21], 0, v[190:191]
	v_lshl_add_u64 v[2:3], v[2:3], 0, v[182:183]
	global_load_dwordx4 v[6:9], v[2:3], off offset:16
	global_load_dwordx4 v[22:25], v[2:3], off
	v_lshl_add_u64 v[2:3], s[20:21], 0, v[192:193]
	v_lshl_add_u64 v[14:15], s[0:1], 0, v[194:195]
	v_lshl_add_u64 v[16:17], s[0:1], 0, v[196:197]
	v_lshl_add_u64 v[10:11], v[2:3], 0, v[182:183]
	v_lshl_add_u64 v[14:15], v[14:15], 0, v[240:241]
	v_lshl_add_u64 v[16:17], v[16:17], 0, v[240:241]
	global_load_dwordx4 v[2:5], v[10:11], off offset:16
	s_nop 0
	global_load_dwordx4 v[10:13], v[10:11], off
	s_nop 0
	global_load_dwordx4 v[18:21], v[14:15], off
	s_nop 0
	global_load_dwordx4 v[14:17], v[16:17], off
	s_waitcnt lgkmcnt(0)
	s_add_i32 s22, s22, 64
	s_add_i32 s29, s29, 0x10000
	s_and_b32 s0, s29, 0x10000
	v_add_u32_e32 v211, s0, v209
	v_add_u32_e32 v242, s0, v210
	s_cmp_lg_u32 s29, 0xe0000
	s_barrier
	s_cbranch_scc1 .LBB1_1
	s_lshl_b64 s[0:1], s[18:19], 24
	ds_read_b128 v[180:183], v210 offset:0
	ds_read_b128 v[184:187], v210 offset:0x800
	ds_read_b128 v[188:191], v210 offset:0x1000
	ds_read_b128 v[192:195], v210 offset:0x1800
	ds_read_b128 v[212:215], v209 offset:0
	ds_read_b128 v[216:219], v209 offset:0x800
	ds_read_b128 v[220:223], v209 offset:0x1000
	s_waitcnt lgkmcnt(0)
	s_add_u32 s0, s10, s0
	s_addc_u32 s18, s11, s1
	s_lshl_b32 s19, s24, 1
	s_mov_b32 s1, 0
	s_add_u32 s0, s0, s19
	s_waitcnt lgkmcnt(2)
	s_addc_u32 s20, s18, 0
	v_mfma_f32_16x16x32_bf16 v[174:177], v[180:183], v[212:215], v[174:177]
	v_mfma_f32_16x16x32_bf16 v[170:173], v[184:187], v[212:215], v[170:173]
	v_mfma_f32_16x16x32_bf16 v[166:169], v[188:191], v[212:215], v[166:169]
	v_mfma_f32_16x16x32_bf16 v[162:165], v[192:195], v[212:215], v[162:165]
	ds_read_b128 v[212:215], v209 offset:0x1800
	s_waitcnt lgkmcnt(2)
	s_nop 0
	v_mfma_f32_16x16x32_bf16 v[158:161], v[180:183], v[216:219], v[158:161]
	v_mfma_f32_16x16x32_bf16 v[154:157], v[184:187], v[216:219], v[154:157]
	v_mfma_f32_16x16x32_bf16 v[150:153], v[188:191], v[216:219], v[150:153]
	v_mfma_f32_16x16x32_bf16 v[146:149], v[192:195], v[216:219], v[146:149]
	ds_read_b128 v[216:219], v209 offset:0x2000
	s_waitcnt lgkmcnt(2)
	s_nop 0
	v_mfma_f32_16x16x32_bf16 v[142:145], v[180:183], v[220:223], v[142:145]
	v_mfma_f32_16x16x32_bf16 v[138:141], v[184:187], v[220:223], v[138:141]
	v_mfma_f32_16x16x32_bf16 v[134:137], v[188:191], v[220:223], v[134:137]
	v_mfma_f32_16x16x32_bf16 v[130:133], v[192:195], v[220:223], v[130:133]
	ds_read_b128 v[220:223], v209 offset:0x2800
	s_waitcnt lgkmcnt(2)
	s_nop 0
	v_mfma_f32_16x16x32_bf16 v[126:129], v[180:183], v[212:215], v[126:129]
	v_mfma_f32_16x16x32_bf16 v[122:125], v[184:187], v[212:215], v[122:125]
	v_mfma_f32_16x16x32_bf16 v[118:121], v[188:191], v[212:215], v[118:121]
	v_mfma_f32_16x16x32_bf16 v[114:117], v[192:195], v[212:215], v[114:117]
	ds_read_b128 v[212:215], v209 offset:0x3000
	s_waitcnt lgkmcnt(2)
	s_nop 0
	v_mfma_f32_16x16x32_bf16 v[110:113], v[180:183], v[216:219], v[110:113]
	v_mfma_f32_16x16x32_bf16 v[106:109], v[184:187], v[216:219], v[106:109]
	v_mfma_f32_16x16x32_bf16 v[102:105], v[188:191], v[216:219], v[102:105]
	v_mfma_f32_16x16x32_bf16 v[98:101], v[192:195], v[216:219], v[98:101]
	ds_read_b128 v[216:219], v209 offset:0x3800
	s_waitcnt lgkmcnt(2)
	s_nop 0
	v_mfma_f32_16x16x32_bf16 v[94:97], v[180:183], v[220:223], v[94:97]
	v_mfma_f32_16x16x32_bf16 v[90:93], v[184:187], v[220:223], v[90:93]
	v_mfma_f32_16x16x32_bf16 v[86:89], v[188:191], v[220:223], v[86:89]
	v_mfma_f32_16x16x32_bf16 v[82:85], v[192:195], v[220:223], v[82:85]
	s_waitcnt lgkmcnt(1)
	s_nop 0
	v_mfma_f32_16x16x32_bf16 v[78:81], v[180:183], v[212:215], v[78:81]
	v_mfma_f32_16x16x32_bf16 v[74:77], v[184:187], v[212:215], v[74:77]
	v_mfma_f32_16x16x32_bf16 v[70:73], v[188:191], v[212:215], v[70:73]
	v_mfma_f32_16x16x32_bf16 v[66:69], v[192:195], v[212:215], v[66:69]
	s_waitcnt lgkmcnt(0)
	s_nop 0
	v_mfma_f32_16x16x32_bf16 v[62:65], v[180:183], v[216:219], v[62:65]
	v_mfma_f32_16x16x32_bf16 v[58:61], v[184:187], v[216:219], v[58:61]
	v_mfma_f32_16x16x32_bf16 v[54:57], v[188:191], v[216:219], v[54:57]
	v_mfma_f32_16x16x32_bf16 v[50:53], v[192:195], v[216:219], v[50:53]
	s_add_i32 s18, 0, 0x10000
	s_waitcnt vmcnt(10)
	v_cvt_pk_bf16_f32 v46, v46, v47
	v_cvt_pk_bf16_f32 v47, v48, v49
	v_cvt_pk_bf16_f32 v48, v42, v43
	v_add_u32_e32 v42, s18, v208
	s_waitcnt vmcnt(8)
	v_cvt_pk_bf16_f32 v38, v38, v39
	v_cvt_pk_bf16_f32 v39, v40, v41
	v_cvt_pk_bf16_f32 v40, v34, v35
	v_add_u32_e32 v34, s18, v205
	s_add_i32 s19, 0, 0x18000
	v_cvt_pk_bf16_f32 v49, v44, v45
	ds_write_b128 v42, v[46:49]
	v_cvt_pk_bf16_f32 v41, v36, v37
	ds_write_b128 v34, v[38:41]
	v_add_u32_e32 v34, s19, v206
	s_waitcnt vmcnt(7)
	ds_write_b128 v34, v[30:33]
	v_add_u32_e32 v30, s19, v207
	s_waitcnt vmcnt(6)
	ds_write_b128 v30, v[26:29]
	ds_read_b128 v[26:29], v210 offset:0x400
	ds_read_b128 v[30:33], v210 offset:0xc00
	ds_read_b128 v[34:37], v210 offset:0x1400
	ds_read_b128 v[38:41], v210 offset:0x1c00
	ds_read_b128 v[42:45], v209 offset:0x400
	ds_read_b128 v[46:49], v209 offset:0xc00
	ds_read_b128 v[180:183], v209 offset:0x1400
	s_nop 0
	s_waitcnt lgkmcnt(2)
	s_nop 0
	v_mfma_f32_16x16x32_bf16 v[174:177], v[26:29], v[42:45], v[174:177]
	v_mfma_f32_16x16x32_bf16 v[170:173], v[30:33], v[42:45], v[170:173]
	v_mfma_f32_16x16x32_bf16 v[166:169], v[34:37], v[42:45], v[166:169]
	v_mfma_f32_16x16x32_bf16 v[42:45], v[38:41], v[42:45], v[162:165]
	ds_read_b128 v[162:165], v209 offset:0x1c00
	s_waitcnt lgkmcnt(2)
	s_nop 0
	v_mfma_f32_16x16x32_bf16 v[158:161], v[26:29], v[46:49], v[158:161]
	v_mfma_f32_16x16x32_bf16 v[154:157], v[30:33], v[46:49], v[154:157]
	v_mfma_f32_16x16x32_bf16 v[150:153], v[34:37], v[46:49], v[150:153]
	v_mfma_f32_16x16x32_bf16 v[46:49], v[38:41], v[46:49], v[146:149]
	ds_read_b128 v[146:149], v209 offset:0x2400
	s_waitcnt lgkmcnt(2)
	s_nop 0
	v_mfma_f32_16x16x32_bf16 v[142:145], v[26:29], v[180:183], v[142:145]
	v_mfma_f32_16x16x32_bf16 v[138:141], v[30:33], v[180:183], v[138:141]
	v_mfma_f32_16x16x32_bf16 v[134:137], v[34:37], v[180:183], v[134:137]
	v_mfma_f32_16x16x32_bf16 v[130:133], v[38:41], v[180:183], v[130:133]
	ds_read_b128 v[180:183], v209 offset:0x2c00
	s_waitcnt lgkmcnt(2)
	s_nop 0
	v_mfma_f32_16x16x32_bf16 v[126:129], v[26:29], v[162:165], v[126:129]
	v_mfma_f32_16x16x32_bf16 v[122:125], v[30:33], v[162:165], v[122:125]
	v_mfma_f32_16x16x32_bf16 v[118:121], v[34:37], v[162:165], v[118:121]
	v_mfma_f32_16x16x32_bf16 v[114:117], v[38:41], v[162:165], v[114:117]
	ds_read_b128 v[162:165], v209 offset:0x3400
	s_waitcnt lgkmcnt(2)
	s_nop 0
	v_mfma_f32_16x16x32_bf16 v[110:113], v[26:29], v[146:149], v[110:113]
	v_mfma_f32_16x16x32_bf16 v[106:109], v[30:33], v[146:149], v[106:109]
	v_mfma_f32_16x16x32_bf16 v[102:105], v[34:37], v[146:149], v[102:105]
	v_mfma_f32_16x16x32_bf16 v[98:101], v[38:41], v[146:149], v[98:101]
	ds_read_b128 v[146:149], v209 offset:0x3c00
	s_waitcnt lgkmcnt(2)
	s_nop 0
	v_mfma_f32_16x16x32_bf16 v[94:97], v[26:29], v[180:183], v[94:97]
	v_mfma_f32_16x16x32_bf16 v[90:93], v[30:33], v[180:183], v[90:93]
	v_mfma_f32_16x16x32_bf16 v[86:89], v[34:37], v[180:183], v[86:89]
	v_mfma_f32_16x16x32_bf16 v[82:85], v[38:41], v[180:183], v[82:85]
	s_waitcnt lgkmcnt(1)
	s_nop 0
	v_mfma_f32_16x16x32_bf16 v[78:81], v[26:29], v[162:165], v[78:81]
	v_mfma_f32_16x16x32_bf16 v[74:77], v[30:33], v[162:165], v[74:77]
	v_mfma_f32_16x16x32_bf16 v[70:73], v[34:37], v[162:165], v[70:73]
	v_mfma_f32_16x16x32_bf16 v[66:69], v[38:41], v[162:165], v[66:69]
	s_waitcnt lgkmcnt(0)
	s_nop 0
	v_mfma_f32_16x16x32_bf16 v[26:29], v[26:29], v[146:149], v[62:65]
	v_mfma_f32_16x16x32_bf16 v[30:33], v[30:33], v[146:149], v[58:61]
	v_mfma_f32_16x16x32_bf16 v[34:37], v[34:37], v[146:149], v[54:57]
	v_mfma_f32_16x16x32_bf16 v[38:41], v[38:41], v[146:149], v[50:53]
	s_waitcnt vmcnt(4)
	v_cvt_pk_bf16_f32 v22, v22, v23
	v_cvt_pk_bf16_f32 v23, v24, v25
	v_cvt_pk_bf16_f32 v24, v6, v7
	v_cvt_pk_bf16_f32 v25, v8, v9
	v_add_u32_e32 v6, s18, v204
	s_waitcnt vmcnt(3)
	v_cvt_pk_bf16_f32 v8, v2, v3
	v_add_u32_e32 v2, s18, v201
	ds_write_b128 v6, v[22:25]
	s_waitcnt vmcnt(2)
	v_cvt_pk_bf16_f32 v6, v10, v11
	v_cvt_pk_bf16_f32 v7, v12, v13
	v_cvt_pk_bf16_f32 v9, v4, v5
	ds_write_b128 v2, v[6:9]
	v_add_u32_e32 v2, s19, v202
	s_waitcnt vmcnt(1)
	ds_write_b128 v2, v[18:21]
	v_add_u32_e32 v2, s19, v203
	s_waitcnt vmcnt(0)
	ds_write_b128 v2, v[14:17]
	s_waitcnt lgkmcnt(0)
	s_barrier
	v_add_u32_e32 v178, 0x10000, v209
	v_add_u32_e32 v196, 0x10000, v210
	ds_read_b128 v[2:5], v196 offset:0
	ds_read_b128 v[6:9], v196 offset:0x800
	ds_read_b128 v[10:13], v196 offset:0x1000
	ds_read_b128 v[14:17], v196 offset:0x1800
	ds_read_b128 v[18:21], v178 offset:0
	s_and_b64 s[16:17], s[16:17], exec
	ds_read_b128 v[22:25], v178 offset:0x800
	ds_read_b128 v[50:53], v178 offset:0x1000
	s_waitcnt lgkmcnt(2)
	s_cselect_b32 s5, s5, s7
	s_cselect_b32 s4, s4, s6
	s_lshl_b32 s6, s3, 10
	v_mfma_f32_16x16x32_bf16 v[54:57], v[2:5], v[18:21], v[174:177]
	s_add_u32 s6, s4, s6
	s_addc_u32 s7, s5, 0
	s_lshl_b32 s3, s3, 9
	v_mfma_f32_16x16x32_bf16 v[58:61], v[6:9], v[18:21], v[170:173]
	s_add_u32 s4, s0, s3
	s_addc_u32 s5, s20, 0
	v_mfma_f32_16x16x32_bf16 v[62:65], v[10:13], v[18:21], v[166:169]
	v_mfma_f32_16x16x32_bf16 v[18:21], v[14:17], v[18:21], v[42:45]
	ds_read_b128 v[42:45], v178 offset:0x1800
	s_waitcnt lgkmcnt(2)
	s_nop 0
	v_mfma_f32_16x16x32_bf16 v[146:149], v[2:5], v[22:25], v[158:161]
	v_mfma_f32_16x16x32_bf16 v[154:157], v[6:9], v[22:25], v[154:157]
	v_mfma_f32_16x16x32_bf16 v[150:153], v[10:13], v[22:25], v[150:153]
	v_mfma_f32_16x16x32_bf16 v[22:25], v[14:17], v[22:25], v[46:49]
	ds_read_b128 v[46:49], v178 offset:0x2000
	s_waitcnt lgkmcnt(2)
	s_nop 0
	v_mfma_f32_16x16x32_bf16 v[142:145], v[2:5], v[50:53], v[142:145]
	v_mfma_f32_16x16x32_bf16 v[138:141], v[6:9], v[50:53], v[138:141]
	v_mfma_f32_16x16x32_bf16 v[134:137], v[10:13], v[50:53], v[134:137]
	v_mfma_f32_16x16x32_bf16 v[50:53], v[14:17], v[50:53], v[130:133]
	ds_read_b128 v[130:133], v178 offset:0x2800
	s_waitcnt lgkmcnt(2)
	s_nop 0
	v_mfma_f32_16x16x32_bf16 v[126:129], v[2:5], v[42:45], v[126:129]
	v_mfma_f32_16x16x32_bf16 v[122:125], v[6:9], v[42:45], v[122:125]
	v_mfma_f32_16x16x32_bf16 v[118:121], v[10:13], v[42:45], v[118:121]
	v_mfma_f32_16x16x32_bf16 v[42:45], v[14:17], v[42:45], v[114:117]
	ds_read_b128 v[114:117], v178 offset:0x3000
	s_waitcnt lgkmcnt(2)
	s_nop 0
	v_mfma_f32_16x16x32_bf16 v[110:113], v[2:5], v[46:49], v[110:113]
	v_mfma_f32_16x16x32_bf16 v[106:109], v[6:9], v[46:49], v[106:109]
	v_mfma_f32_16x16x32_bf16 v[102:105], v[10:13], v[46:49], v[102:105]
	v_mfma_f32_16x16x32_bf16 v[98:101], v[14:17], v[46:49], v[98:101]
	ds_read_b128 v[46:49], v178 offset:0x3800
	s_waitcnt lgkmcnt(2)
	s_nop 0
	v_mfma_f32_16x16x32_bf16 v[158:161], v[2:5], v[130:133], v[94:97]
	v_mfma_f32_16x16x32_bf16 v[162:165], v[6:9], v[130:133], v[90:93]
	v_mfma_f32_16x16x32_bf16 v[166:169], v[10:13], v[130:133], v[86:89]
	v_mfma_f32_16x16x32_bf16 v[130:133], v[14:17], v[130:133], v[82:85]
	s_waitcnt lgkmcnt(1)
	s_nop 0
	v_mfma_f32_16x16x32_bf16 v[66:69], v[14:17], v[114:117], v[66:69]
	v_mfma_f32_16x16x32_bf16 v[170:173], v[2:5], v[114:117], v[78:81]
	v_mfma_f32_16x16x32_bf16 v[174:177], v[6:9], v[114:117], v[74:77]
	v_mfma_f32_16x16x32_bf16 v[180:183], v[10:13], v[114:117], v[70:73]
	s_waitcnt lgkmcnt(0)
	s_nop 0
	v_mfma_f32_16x16x32_bf16 v[2:5], v[2:5], v[46:49], v[26:29]
	v_mfma_f32_16x16x32_bf16 v[114:117], v[6:9], v[46:49], v[30:33]
	v_mfma_f32_16x16x32_bf16 v[34:37], v[10:13], v[46:49], v[34:37]
	v_mfma_f32_16x16x32_bf16 v[184:187], v[14:17], v[46:49], v[38:41]
	ds_read_b128 v[188:191], v196 offset:0x400
	ds_read_b128 v[192:195], v196 offset:0xc00
	ds_read_b128 v[202:205], v196 offset:0x1400
	ds_read_b128 v[206:209], v196 offset:0x1c00
	ds_read_b128 v[6:9], v178 offset:0x400
	ds_read_b128 v[10:13], v178 offset:0xc00
	ds_read_b128 v[14:17], v178 offset:0x1400
	s_nop 0
	s_waitcnt lgkmcnt(2)
	s_nop 0
	v_mfma_f32_16x16x32_bf16 v[94:97], v[192:195], v[6:9], v[58:61]
	v_mfma_f32_16x16x32_bf16 v[62:65], v[202:205], v[6:9], v[62:65]
	v_mfma_f32_16x16x32_bf16 v[30:33], v[206:209], v[6:9], v[18:21]
	v_mfma_f32_16x16x32_bf16 v[210:213], v[188:191], v[6:9], v[54:57]
	ds_read_b128 v[6:9], v178 offset:0x1c00
	s_waitcnt lgkmcnt(2)
	s_nop 0
	v_mfma_f32_16x16x32_bf16 v[90:93], v[192:195], v[10:13], v[154:157]
	v_mfma_f32_16x16x32_bf16 v[58:61], v[202:205], v[10:13], v[150:153]
	v_mfma_f32_16x16x32_bf16 v[26:29], v[206:209], v[10:13], v[22:25]
	v_mfma_f32_16x16x32_bf16 v[146:149], v[188:191], v[10:13], v[146:149]
	ds_read_b128 v[10:13], v178 offset:0x2400
	s_waitcnt lgkmcnt(2)
	s_nop 0
	v_mfma_f32_16x16x32_bf16 v[86:89], v[192:195], v[14:17], v[138:141]
	v_mfma_f32_16x16x32_bf16 v[54:57], v[202:205], v[14:17], v[134:137]
	v_mfma_f32_16x16x32_bf16 v[22:25], v[206:209], v[14:17], v[50:53]
	v_mfma_f32_16x16x32_bf16 v[142:145], v[188:191], v[14:17], v[142:145]
	ds_read_b128 v[38:41], v178 offset:0x2c00
	s_waitcnt lgkmcnt(2)
	s_nop 0
	v_mfma_f32_16x16x32_bf16 v[126:129], v[188:191], v[6:9], v[126:129]
	v_mfma_f32_16x16x32_bf16 v[82:85], v[192:195], v[6:9], v[122:125]
	v_mfma_f32_16x16x32_bf16 v[50:53], v[202:205], v[6:9], v[118:121]
	v_mfma_f32_16x16x32_bf16 v[18:21], v[206:209], v[6:9], v[42:45]
	ds_read_b128 v[6:9], v178 offset:0x3400
	s_waitcnt lgkmcnt(2)
	s_nop 0
	v_mfma_f32_16x16x32_bf16 v[110:113], v[188:191], v[10:13], v[110:113]
	v_mfma_f32_16x16x32_bf16 v[78:81], v[192:195], v[10:13], v[106:109]
	v_mfma_f32_16x16x32_bf16 v[46:49], v[202:205], v[10:13], v[102:105]
	v_mfma_f32_16x16x32_bf16 v[14:17], v[206:209], v[10:13], v[98:101]
	ds_read_b128 v[98:101], v178 offset:0x3c00
	s_waitcnt lgkmcnt(2)
	s_nop 0
	v_mfma_f32_16x16x32_bf16 v[106:109], v[188:191], v[38:41], v[158:161]
	v_mfma_f32_16x16x32_bf16 v[74:77], v[192:195], v[38:41], v[162:165]
	v_mfma_f32_16x16x32_bf16 v[42:45], v[202:205], v[38:41], v[166:169]
	v_mfma_f32_16x16x32_bf16 v[10:13], v[206:209], v[38:41], v[130:133]
	s_waitcnt lgkmcnt(1)
	s_nop 0
	v_mfma_f32_16x16x32_bf16 v[118:121], v[188:191], v[6:9], v[170:173]
	v_mfma_f32_16x16x32_bf16 v[70:73], v[192:195], v[6:9], v[174:177]
	v_mfma_f32_16x16x32_bf16 v[38:41], v[202:205], v[6:9], v[180:183]
	v_mfma_f32_16x16x32_bf16 v[6:9], v[206:209], v[6:9], v[66:69]
	s_waitcnt lgkmcnt(0)
	s_nop 0
	v_mfma_f32_16x16x32_bf16 v[122:125], v[188:191], v[98:101], v[2:5]
	v_mfma_f32_16x16x32_bf16 v[66:69], v[192:195], v[98:101], v[114:117]
	v_mfma_f32_16x16x32_bf16 v[34:37], v[202:205], v[98:101], v[34:37]
	v_mfma_f32_16x16x32_bf16 v[2:5], v[206:209], v[98:101], v[184:187]
	v_lshrrev_b32_e32 v98, 2, v199
	v_and_b32_e32 v98, 12, v98
	v_lshl_or_b32 v104, v200, 6, v98
	v_lshlrev_b32_e32 v105, 2, v104
	s_waitcnt lgkmcnt(0)
	s_barrier
	global_load_dwordx4 v[114:117], v105, s[6:7]
	v_lshrrev_b32_e32 v98, 1, v199
	v_lshlrev_b32_e32 v99, 16, v198
	v_lshlrev_b32_e32 v100, 9, v179
	v_and_b32_e32 v102, 8, v98
	v_lshrrev_b32_e32 v98, 3, v104
	v_add3_u32 v103, 0, v99, v100
	v_xor_b32_e32 v130, v98, v179
	v_bitop3_b32 v131, v98, v179, 16 bitop3:0x1e
	global_load_dwordx4 v[98:101], v105, s[6:7] offset:64
	v_lshlrev_b32_e32 v130, 4, v130
	v_lshlrev_b32_e32 v131, 4, v131
	v_add3_u32 v130, v103, v130, v102
	v_add3_u32 v131, v103, v131, v102
	s_movk_i32 s0, 0x200
	s_waitcnt vmcnt(1)
	v_add_f32_e32 v132, v210, v114
	v_add_f32_e32 v133, v211, v115
	v_add_f32_e32 v134, v212, v116
	v_add_f32_e32 v135, v213, v117
	v_add_f32_e32 v140, v142, v114
	v_add_f32_e32 v141, v143, v115
	v_add_f32_e32 v142, v144, v116
	v_add_f32_e32 v143, v145, v117
	v_add_f32_e32 v110, v110, v114
	v_add_f32_e32 v111, v111, v115
	v_add_f32_e32 v106, v106, v114
	v_add_f32_e32 v107, v107, v115
	v_add_f32_e32 v136, v146, v114
	v_add_f32_e32 v137, v147, v115
	v_add_f32_e32 v138, v148, v116
	v_add_f32_e32 v139, v149, v117
	v_add_f32_e32 v126, v126, v114
	v_add_f32_e32 v127, v127, v115
	v_add_f32_e32 v128, v128, v116
	v_add_f32_e32 v129, v129, v117
	v_add_f32_e32 v112, v112, v116
	v_add_f32_e32 v113, v113, v117
	v_add_f32_e32 v108, v108, v116
	v_add_f32_e32 v109, v109, v117
	v_max_f32_e32 v132, 0, v132
	v_max_f32_e32 v133, 0, v133
	v_max_f32_e32 v134, 0, v134
	v_max_f32_e32 v135, 0, v135
	v_max_f32_e32 v140, 0, v140
	v_max_f32_e32 v141, 0, v141
	v_max_f32_e32 v142, 0, v142
	v_max_f32_e32 v143, 0, v143
	v_max_f32_e32 v144, 0, v110
	v_max_f32_e32 v145, 0, v111
	v_max_f32_e32 v148, 0, v106
	v_max_f32_e32 v149, 0, v107
	v_cvt_pk_bf16_f32 v106, v132, v133
	v_cvt_pk_bf16_f32 v107, v134, v135
	v_cvt_pk_bf16_f32 v110, v140, v141
	v_cvt_pk_bf16_f32 v111, v142, v143
	v_add_f32_e32 v118, v118, v114
	v_add_f32_e32 v119, v119, v115
	v_max_f32_e32 v136, 0, v136
	v_max_f32_e32 v137, 0, v137
	v_max_f32_e32 v138, 0, v138
	v_max_f32_e32 v139, 0, v139
	v_max_f32_e32 v126, 0, v126
	v_max_f32_e32 v127, 0, v127
	v_max_f32_e32 v128, 0, v128
	v_max_f32_e32 v129, 0, v129
	v_max_f32_e32 v146, 0, v112
	v_max_f32_e32 v147, 0, v113
	v_max_f32_e32 v150, 0, v108
	v_max_f32_e32 v151, 0, v109
	v_cvt_pk_bf16_f32 v108, v136, v137
	v_cvt_pk_bf16_f32 v109, v138, v139
	v_cvt_pk_bf16_f32 v112, v126, v127
	v_cvt_pk_bf16_f32 v113, v128, v129
	ds_write2st64_b64 v130, v[106:107], v[110:111] offset1:32
	ds_write2st64_b64 v131, v[108:109], v[112:113] offset0:16 offset1:48
	v_add_f32_e32 v106, v121, v117
	v_add_f32_e32 v120, v120, v116
	v_max_f32_e32 v152, 0, v118
	v_max_f32_e32 v153, 0, v119
	v_max_f32_e32 v107, 0, v106
	v_cvt_pk_bf16_f32 v106, v152, v153
	v_max_f32_e32 v120, 0, v120
	v_cvt_pk_bf16_f32 v118, v144, v145
	v_cvt_pk_bf16_f32 v119, v146, v147
	v_cvt_pk_bf16_f32 v107, v120, v107
	ds_write2st64_b64 v130, v[118:119], v[106:107] offset0:64 offset1:96
	v_add_f32_e32 v106, v122, v114
	v_max_f32_e32 v106, 0, v106
	v_add_f32_e32 v107, v123, v115
	v_max_f32_e32 v107, 0, v107
	v_add_f32_e32 v108, v124, v116
	v_add_f32_e32 v109, v125, v117
	v_cvt_pk_bf16_f32 v106, v106, v107
	v_cvt_pk_bf16_f32 v126, v148, v149
	v_cvt_pk_bf16_f32 v127, v150, v151
	v_max_f32_e32 v108, 0, v108
	v_max_f32_e32 v109, 0, v109
	v_cvt_pk_bf16_f32 v107, v108, v109
	ds_write2st64_b64 v131, v[126:127], v[106:107] offset0:80 offset1:112
	v_or_b32_e32 v106, 16, v104
	s_waitcnt vmcnt(0)
	v_add_f32_e32 v94, v94, v98
	v_add_f32_e32 v95, v95, v99
	v_add_f32_e32 v96, v96, v100
	v_lshrrev_b32_e32 v106, 3, v106
	v_max_f32_e32 v94, 0, v94
	v_max_f32_e32 v95, 0, v95
	v_max_f32_e32 v96, 0, v96
	v_add_f32_e32 v97, v97, v101
	v_max_f32_e32 v97, 0, v97
	v_cvt_pk_bf16_f32 v94, v94, v95
	v_cvt_pk_bf16_f32 v95, v96, v97
	v_xor_b32_e32 v96, v106, v179
	v_lshlrev_b32_e32 v96, 4, v96
	v_add3_u32 v107, v103, v96, v102
	v_add_f32_e32 v90, v90, v98
	v_add_f32_e32 v91, v91, v99
	v_add_f32_e32 v92, v92, v100
	ds_write_b64 v107, v[94:95]
	v_max_f32_e32 v90, 0, v90
	v_max_f32_e32 v91, 0, v91
	global_load_dwordx4 v[94:97], v105, s[6:7] offset:128
	v_max_f32_e32 v92, 0, v92
	v_add_f32_e32 v93, v93, v101
	v_max_f32_e32 v93, 0, v93
	v_cvt_pk_bf16_f32 v90, v90, v91
	v_cvt_pk_bf16_f32 v91, v92, v93
	v_bitop3_b32 v92, v106, v179, 16 bitop3:0x1e
	v_add_f32_e32 v66, v66, v98
	v_lshlrev_b32_e32 v92, 4, v92
	v_add_f32_e32 v86, v86, v98
	v_add_f32_e32 v87, v87, v99
	v_add_f32_e32 v82, v82, v98
	v_add_f32_e32 v83, v83, v99
	v_add_f32_e32 v78, v78, v98
	v_add_f32_e32 v79, v79, v99
	v_add_f32_e32 v74, v74, v98
	v_add_f32_e32 v75, v75, v99
	v_add_f32_e32 v70, v70, v98
	v_add_f32_e32 v71, v71, v99
	v_max_f32_e32 v66, 0, v66
	v_add_f32_e32 v67, v67, v99
	v_add3_u32 v92, v103, v92, v102
	v_max_f32_e32 v86, 0, v86
	v_max_f32_e32 v87, 0, v87
	v_add_f32_e32 v88, v88, v100
	v_add_f32_e32 v89, v89, v101
	v_max_f32_e32 v82, 0, v82
	v_max_f32_e32 v83, 0, v83
	v_add_f32_e32 v84, v84, v100
	v_add_f32_e32 v85, v85, v101
	v_max_f32_e32 v78, 0, v78
	v_max_f32_e32 v79, 0, v79
	v_add_f32_e32 v80, v80, v100
	v_add_f32_e32 v81, v81, v101
	v_max_f32_e32 v74, 0, v74
	v_max_f32_e32 v75, 0, v75
	v_add_f32_e32 v76, v76, v100
	v_add_f32_e32 v77, v77, v101
	v_max_f32_e32 v70, 0, v70
	v_max_f32_e32 v71, 0, v71
	v_add_f32_e32 v72, v72, v100
	v_add_f32_e32 v73, v73, v101
	v_max_f32_e32 v67, 0, v67
	v_add_f32_e32 v68, v68, v100
	v_add_f32_e32 v69, v69, v101
	v_cvt_pk_bf16_f32 v66, v66, v67
	ds_write_b64 v92, v[90:91] offset:8192
	v_max_f32_e32 v88, 0, v88
	v_max_f32_e32 v89, 0, v89
	v_cvt_pk_bf16_f32 v86, v86, v87
	v_cvt_pk_bf16_f32 v87, v88, v89
	ds_write_b64 v107, v[86:87] offset:16384
	v_max_f32_e32 v84, 0, v84
	v_max_f32_e32 v85, 0, v85
	v_cvt_pk_bf16_f32 v82, v82, v83
	v_cvt_pk_bf16_f32 v83, v84, v85
	ds_write_b64 v92, v[82:83] offset:24576
	v_max_f32_e32 v80, 0, v80
	v_max_f32_e32 v81, 0, v81
	v_cvt_pk_bf16_f32 v78, v78, v79
	v_cvt_pk_bf16_f32 v79, v80, v81
	ds_write_b64 v107, v[78:79] offset:32768
	v_max_f32_e32 v76, 0, v76
	v_max_f32_e32 v77, 0, v77
	v_cvt_pk_bf16_f32 v74, v74, v75
	v_cvt_pk_bf16_f32 v75, v76, v77
	ds_write_b64 v92, v[74:75] offset:40960
	v_max_f32_e32 v72, 0, v72
	v_max_f32_e32 v73, 0, v73
	v_cvt_pk_bf16_f32 v70, v70, v71
	v_cvt_pk_bf16_f32 v71, v72, v73
	ds_write_b64 v107, v[70:71] offset:49152
	v_max_f32_e32 v68, 0, v68
	v_max_f32_e32 v69, 0, v69
	v_cvt_pk_bf16_f32 v67, v68, v69
	ds_write_b64 v92, v[66:67] offset:57344
	v_or_b32_e32 v66, 32, v104
	v_lshrrev_b32_e32 v70, 3, v66
	global_load_dwordx4 v[66:69], v105, s[6:7] offset:192
	s_waitcnt vmcnt(1)
	v_add_f32_e32 v62, v62, v94
	v_add_f32_e32 v63, v63, v95
	v_add_f32_e32 v64, v64, v96
	v_add_f32_e32 v58, v58, v94
	v_add_f32_e32 v59, v59, v95
	v_add_f32_e32 v60, v60, v96
	v_max_f32_e32 v62, 0, v62
	v_max_f32_e32 v63, 0, v63
	v_max_f32_e32 v64, 0, v64
	v_add_f32_e32 v65, v65, v97
	v_max_f32_e32 v58, 0, v58
	v_max_f32_e32 v59, 0, v59
	v_max_f32_e32 v60, 0, v60
	v_add_f32_e32 v61, v61, v97
	v_max_f32_e32 v65, 0, v65
	v_cvt_pk_bf16_f32 v62, v62, v63
	v_cvt_pk_bf16_f32 v63, v64, v65
	v_xor_b32_e32 v64, v70, v179
	v_max_f32_e32 v61, 0, v61
	v_cvt_pk_bf16_f32 v58, v58, v59
	v_cvt_pk_bf16_f32 v59, v60, v61
	v_bitop3_b32 v60, v70, v179, 16 bitop3:0x1e
	v_add_f32_e32 v34, v34, v94
	v_lshlrev_b32_e32 v64, 4, v64
	v_lshlrev_b32_e32 v60, 4, v60
	v_add_f32_e32 v54, v54, v94
	v_add_f32_e32 v55, v55, v95
	v_add_f32_e32 v50, v50, v94
	v_add_f32_e32 v51, v51, v95
	v_add_f32_e32 v46, v46, v94
	v_add_f32_e32 v47, v47, v95
	v_add_f32_e32 v42, v42, v94
	v_add_f32_e32 v43, v43, v95
	v_add_f32_e32 v38, v38, v94
	v_add_f32_e32 v39, v39, v95
	v_max_f32_e32 v34, 0, v34
	v_add_f32_e32 v35, v35, v95
	v_add3_u32 v64, v103, v64, v102
	v_add3_u32 v60, v103, v60, v102
	v_max_f32_e32 v54, 0, v54
	v_max_f32_e32 v55, 0, v55
	v_add_f32_e32 v56, v56, v96
	v_add_f32_e32 v57, v57, v97
	v_max_f32_e32 v50, 0, v50
	v_max_f32_e32 v51, 0, v51
	v_add_f32_e32 v52, v52, v96
	v_add_f32_e32 v53, v53, v97
	v_max_f32_e32 v46, 0, v46
	v_max_f32_e32 v47, 0, v47
	v_add_f32_e32 v48, v48, v96
	v_add_f32_e32 v49, v49, v97
	v_max_f32_e32 v42, 0, v42
	v_max_f32_e32 v43, 0, v43
	v_add_f32_e32 v44, v44, v96
	v_add_f32_e32 v45, v45, v97
	v_max_f32_e32 v38, 0, v38
	v_max_f32_e32 v39, 0, v39
	v_add_f32_e32 v40, v40, v96
	v_add_f32_e32 v41, v41, v97
	v_max_f32_e32 v35, 0, v35
	v_add_f32_e32 v36, v36, v96
	v_add_f32_e32 v37, v37, v97
	v_cvt_pk_bf16_f32 v34, v34, v35
	ds_write_b64 v64, v[62:63]
	ds_write_b64 v60, v[58:59] offset:8192
	v_max_f32_e32 v56, 0, v56
	v_max_f32_e32 v57, 0, v57
	v_cvt_pk_bf16_f32 v54, v54, v55
	v_cvt_pk_bf16_f32 v55, v56, v57
	ds_write_b64 v64, v[54:55] offset:16384
	v_max_f32_e32 v52, 0, v52
	v_max_f32_e32 v53, 0, v53
	v_cvt_pk_bf16_f32 v50, v50, v51
	v_cvt_pk_bf16_f32 v51, v52, v53
	ds_write_b64 v60, v[50:51] offset:24576
	v_max_f32_e32 v48, 0, v48
	v_max_f32_e32 v49, 0, v49
	v_cvt_pk_bf16_f32 v46, v46, v47
	v_cvt_pk_bf16_f32 v47, v48, v49
	ds_write_b64 v64, v[46:47] offset:32768
	v_max_f32_e32 v44, 0, v44
	v_max_f32_e32 v45, 0, v45
	v_cvt_pk_bf16_f32 v42, v42, v43
	v_cvt_pk_bf16_f32 v43, v44, v45
	ds_write_b64 v60, v[42:43] offset:40960
	v_max_f32_e32 v40, 0, v40
	v_max_f32_e32 v41, 0, v41
	v_cvt_pk_bf16_f32 v38, v38, v39
	v_cvt_pk_bf16_f32 v39, v40, v41
	ds_write_b64 v64, v[38:39] offset:49152
	v_max_f32_e32 v36, 0, v36
	v_max_f32_e32 v37, 0, v37
	v_cvt_pk_bf16_f32 v35, v36, v37
	ds_write_b64 v60, v[34:35] offset:57344
	v_or_b32_e32 v34, 48, v104
	s_waitcnt vmcnt(0)
	v_add_f32_e32 v30, v30, v66
	v_add_f32_e32 v31, v31, v67
	v_add_f32_e32 v32, v32, v68
	v_add_f32_e32 v26, v26, v66
	v_add_f32_e32 v27, v27, v67
	v_add_f32_e32 v28, v28, v68
	v_lshrrev_b32_e32 v34, 3, v34
	v_max_f32_e32 v30, 0, v30
	v_max_f32_e32 v31, 0, v31
	v_max_f32_e32 v32, 0, v32
	v_add_f32_e32 v33, v33, v69
	v_max_f32_e32 v26, 0, v26
	v_max_f32_e32 v27, 0, v27
	v_max_f32_e32 v28, 0, v28
	v_add_f32_e32 v29, v29, v69
	v_max_f32_e32 v33, 0, v33
	v_cvt_pk_bf16_f32 v30, v30, v31
	v_cvt_pk_bf16_f32 v31, v32, v33
	v_xor_b32_e32 v32, v34, v179
	v_max_f32_e32 v29, 0, v29
	v_cvt_pk_bf16_f32 v26, v26, v27
	v_cvt_pk_bf16_f32 v27, v28, v29
	v_bitop3_b32 v28, v34, v179, 16 bitop3:0x1e
	v_add_f32_e32 v2, v2, v66
	v_lshlrev_b32_e32 v32, 4, v32
	v_lshlrev_b32_e32 v28, 4, v28
	v_add_f32_e32 v22, v22, v66
	v_add_f32_e32 v23, v23, v67
	v_add_f32_e32 v18, v18, v66
	v_add_f32_e32 v19, v19, v67
	v_add_f32_e32 v14, v14, v66
	v_add_f32_e32 v15, v15, v67
	v_add_f32_e32 v10, v10, v66
	v_add_f32_e32 v11, v11, v67
	v_add_f32_e32 v6, v6, v66
	v_add_f32_e32 v7, v7, v67
	v_max_f32_e32 v2, 0, v2
	v_add_f32_e32 v3, v3, v67
	v_add3_u32 v32, v103, v32, v102
	v_add3_u32 v28, v103, v28, v102
	v_max_f32_e32 v22, 0, v22
	v_max_f32_e32 v23, 0, v23
	v_add_f32_e32 v24, v24, v68
	v_add_f32_e32 v25, v25, v69
	v_max_f32_e32 v18, 0, v18
	v_max_f32_e32 v19, 0, v19
	v_add_f32_e32 v20, v20, v68
	v_add_f32_e32 v21, v21, v69
	v_max_f32_e32 v14, 0, v14
	v_max_f32_e32 v15, 0, v15
	v_add_f32_e32 v16, v16, v68
	v_add_f32_e32 v17, v17, v69
	v_max_f32_e32 v10, 0, v10
	v_max_f32_e32 v11, 0, v11
	v_add_f32_e32 v12, v12, v68
	v_add_f32_e32 v13, v13, v69
	v_max_f32_e32 v6, 0, v6
	v_max_f32_e32 v7, 0, v7
	v_add_f32_e32 v8, v8, v68
	v_add_f32_e32 v9, v9, v69
	v_max_f32_e32 v3, 0, v3
	v_add_f32_e32 v4, v4, v68
	v_add_f32_e32 v5, v5, v69
	v_cvt_pk_bf16_f32 v2, v2, v3
	ds_write_b64 v32, v[30:31]
	ds_write_b64 v28, v[26:27] offset:8192
	v_max_f32_e32 v24, 0, v24
	v_max_f32_e32 v25, 0, v25
	v_cvt_pk_bf16_f32 v22, v22, v23
	v_cvt_pk_bf16_f32 v23, v24, v25
	ds_write_b64 v32, v[22:23] offset:16384
	v_max_f32_e32 v20, 0, v20
	v_max_f32_e32 v21, 0, v21
	v_cvt_pk_bf16_f32 v18, v18, v19
	v_cvt_pk_bf16_f32 v19, v20, v21
	ds_write_b64 v28, v[18:19] offset:24576
	v_max_f32_e32 v16, 0, v16
	v_max_f32_e32 v17, 0, v17
	v_cvt_pk_bf16_f32 v14, v14, v15
	v_cvt_pk_bf16_f32 v15, v16, v17
	ds_write_b64 v32, v[14:15] offset:32768
	v_max_f32_e32 v12, 0, v12
	v_max_f32_e32 v13, 0, v13
	v_cvt_pk_bf16_f32 v10, v10, v11
	v_cvt_pk_bf16_f32 v11, v12, v13
	ds_write_b64 v28, v[10:11] offset:40960
	v_max_f32_e32 v8, 0, v8
	v_max_f32_e32 v9, 0, v9
	v_cvt_pk_bf16_f32 v6, v6, v7
	v_cvt_pk_bf16_f32 v7, v8, v9
	ds_write_b64 v32, v[6:7] offset:49152
	v_max_f32_e32 v4, 0, v4
	v_max_f32_e32 v5, 0, v5
	v_cvt_pk_bf16_f32 v3, v4, v5
	ds_write_b64 v28, v[2:3] offset:57344
	v_and_b32_e32 v2, 0x1f0, v1
	v_lshrrev_b32_e32 v1, 5, v0
	v_xor_b32_e32 v4, v1, v0
	v_mov_b32_e32 v3, 0
	v_lshlrev_b32_e32 v4, 4, v4
	v_lshl_add_u64 v[12:13], s[4:5], 0, v[2:3]
	v_lshlrev_b32_e32 v2, 9, v1
	v_and_b32_e32 v16, 0x1f0, v4
	v_add3_u32 v2, 0, v2, v16
	s_waitcnt lgkmcnt(0)
	s_barrier
	ds_read_b128 v[4:7], v2
	v_lshlrev_b32_e32 v2, 11, v1
	v_lshl_add_u64 v[14:15], v[12:13], 0, v[2:3]
	v_or_b32_e32 v2, 0x200, v0
	v_lshrrev_b32_e32 v2, 5, v2
	v_xor_b32_e32 v9, v2, v0
	v_lshlrev_b32_e32 v9, 4, v9
	v_lshlrev_b32_e32 v8, 9, v2
	v_and_b32_e32 v9, 0x1f0, v9
	v_add3_u32 v8, 0, v8, v9
	ds_read_b128 v[8:11], v8
	v_lshlrev_b32_e32 v2, 11, v2
	s_waitcnt lgkmcnt(1)
	global_store_dwordx4 v[14:15], v[4:7], off sc1
	s_nop 1
	v_lshl_add_u64 v[4:5], v[12:13], 0, v[2:3]
	s_waitcnt lgkmcnt(0)
	global_store_dwordx4 v[4:5], v[8:11], off sc1
	v_or_b32_e32 v2, 32, v1
	v_lshlrev_b32_e32 v4, 9, v2
	v_or_b32_e32 v8, 0x600, v0
	v_lshrrev_b32_e32 v17, 5, v8
	v_xor_b32_e32 v9, v17, v0
	v_lshlrev_b32_e32 v9, 4, v9
	v_add3_u32 v4, 0, v4, v16
	v_lshlrev_b32_e32 v8, 9, v17
	v_and_b32_e32 v9, 0x1f0, v9
	ds_read_b128 v[4:7], v4
	v_add3_u32 v8, 0, v8, v9
	ds_read_b128 v[8:11], v8
	v_lshlrev_b32_e32 v2, 11, v2
	v_lshl_add_u64 v[14:15], v[12:13], 0, v[2:3]
	v_lshlrev_b32_e32 v2, 11, v17
	s_waitcnt lgkmcnt(1)
	global_store_dwordx4 v[14:15], v[4:7], off sc1
	s_nop 1
	v_lshl_add_u64 v[4:5], v[12:13], 0, v[2:3]
	s_waitcnt lgkmcnt(0)
	global_store_dwordx4 v[4:5], v[8:11], off sc1
	v_or_b32_e32 v2, 64, v1
	v_lshlrev_b32_e32 v4, 9, v2
	v_or_b32_e32 v8, 0xa00, v0
	v_lshrrev_b32_e32 v17, 5, v8
	v_xor_b32_e32 v9, v17, v0
	v_lshlrev_b32_e32 v9, 4, v9
	v_add3_u32 v4, 0, v4, v16
	v_lshlrev_b32_e32 v8, 9, v17
	v_and_b32_e32 v9, 0x1f0, v9
	ds_read_b128 v[4:7], v4
	v_add3_u32 v8, 0, v8, v9
	ds_read_b128 v[8:11], v8
	v_lshlrev_b32_e32 v2, 11, v2
	v_lshl_add_u64 v[14:15], v[12:13], 0, v[2:3]
	v_lshlrev_b32_e32 v2, 11, v17
	s_waitcnt lgkmcnt(1)
	global_store_dwordx4 v[14:15], v[4:7], off sc1
	s_nop 1
	v_lshl_add_u64 v[4:5], v[12:13], 0, v[2:3]
	s_waitcnt lgkmcnt(0)
	global_store_dwordx4 v[4:5], v[8:11], off sc1
	v_or_b32_e32 v2, 0x60, v1
	v_lshlrev_b32_e32 v4, 9, v2
	v_or_b32_e32 v8, 0xe00, v0
	v_lshrrev_b32_e32 v17, 5, v8
	v_xor_b32_e32 v9, v17, v0
	v_lshlrev_b32_e32 v9, 4, v9
	v_add3_u32 v4, 0, v4, v16
	v_lshlrev_b32_e32 v8, 9, v17
	v_and_b32_e32 v9, 0x1f0, v9
	ds_read_b128 v[4:7], v4
	v_add3_u32 v8, 0, v8, v9
	ds_read_b128 v[8:11], v8
	v_lshlrev_b32_e32 v2, 11, v2
	v_lshl_add_u64 v[14:15], v[12:13], 0, v[2:3]
	v_lshlrev_b32_e32 v2, 11, v17
	s_waitcnt lgkmcnt(1)
	global_store_dwordx4 v[14:15], v[4:7], off sc1
	s_nop 1
	v_lshl_add_u64 v[4:5], v[12:13], 0, v[2:3]
	s_waitcnt lgkmcnt(0)
	global_store_dwordx4 v[4:5], v[8:11], off sc1
	v_or_b32_e32 v2, 0x80, v1
	v_lshlrev_b32_e32 v4, 9, v2
	v_or_b32_e32 v8, 0x1200, v0
	v_lshrrev_b32_e32 v17, 5, v8
	v_xor_b32_e32 v9, v17, v0
	v_lshlrev_b32_e32 v9, 4, v9
	v_add3_u32 v4, 0, v4, v16
	v_lshlrev_b32_e32 v8, 9, v17
	v_and_b32_e32 v9, 0x1f0, v9
	ds_read_b128 v[4:7], v4
	v_add3_u32 v8, 0, v8, v9
	ds_read_b128 v[8:11], v8
	v_lshlrev_b32_e32 v2, 11, v2
	v_lshl_add_u64 v[14:15], v[12:13], 0, v[2:3]
	v_lshlrev_b32_e32 v2, 11, v17
	s_waitcnt lgkmcnt(1)
	global_store_dwordx4 v[14:15], v[4:7], off sc1
	s_nop 1
	v_lshl_add_u64 v[4:5], v[12:13], 0, v[2:3]
	s_waitcnt lgkmcnt(0)
	global_store_dwordx4 v[4:5], v[8:11], off sc1
	v_or_b32_e32 v2, 0xa0, v1
	v_lshlrev_b32_e32 v4, 9, v2
	v_or_b32_e32 v8, 0x1600, v0
	v_lshrrev_b32_e32 v17, 5, v8
	v_xor_b32_e32 v9, v17, v0
	v_lshlrev_b32_e32 v9, 4, v9
	v_add3_u32 v4, 0, v4, v16
	v_lshlrev_b32_e32 v8, 9, v17
	v_and_b32_e32 v9, 0x1f0, v9
	ds_read_b128 v[4:7], v4
	v_add3_u32 v8, 0, v8, v9
	ds_read_b128 v[8:11], v8
	v_lshlrev_b32_e32 v2, 11, v2
	v_lshl_add_u64 v[14:15], v[12:13], 0, v[2:3]
	v_lshlrev_b32_e32 v2, 11, v17
	s_waitcnt lgkmcnt(1)
	global_store_dwordx4 v[14:15], v[4:7], off sc1
	s_nop 1
	v_lshl_add_u64 v[4:5], v[12:13], 0, v[2:3]
	s_waitcnt lgkmcnt(0)
	global_store_dwordx4 v[4:5], v[8:11], off sc1
	v_or_b32_e32 v2, 0xc0, v1
	v_lshlrev_b32_e32 v4, 9, v2
	v_or_b32_e32 v8, 0x1a00, v0
	v_lshrrev_b32_e32 v17, 5, v8
	v_xor_b32_e32 v9, v17, v0
	v_add3_u32 v4, 0, v4, v16
	v_lshlrev_b32_e32 v9, 4, v9
	ds_read_b128 v[4:7], v4
	v_lshlrev_b32_e32 v8, 9, v17
	v_and_b32_e32 v9, 0x1f0, v9
	v_add3_u32 v8, 0, v8, v9
	ds_read_b128 v[8:11], v8
	v_lshlrev_b32_e32 v2, 11, v2
	v_lshl_add_u64 v[14:15], v[12:13], 0, v[2:3]
	v_lshlrev_b32_e32 v2, 11, v17
	v_or_b32_e32 v1, 0xe0, v1
	s_waitcnt lgkmcnt(1)
	global_store_dwordx4 v[14:15], v[4:7], off sc1
	s_nop 1
	v_lshl_add_u64 v[4:5], v[12:13], 0, v[2:3]
	v_lshlrev_b32_e32 v2, 9, v1
	v_add3_u32 v2, 0, v2, v16
	s_waitcnt lgkmcnt(0)
	global_store_dwordx4 v[4:5], v[8:11], off sc1
	ds_read_b128 v[4:7], v2
	v_lshlrev_b32_e32 v2, 11, v1
	v_or_b32_e32 v1, 0x1e00, v0
	v_lshrrev_b32_e32 v1, 5, v1
	v_xor_b32_e32 v9, v1, v0
	v_lshlrev_b32_e32 v9, 4, v9
	v_lshlrev_b32_e32 v8, 9, v1
	v_and_b32_e32 v9, 0x1f0, v9
	v_add3_u32 v8, 0, v8, v9
	ds_read_b128 v[8:11], v8
	v_lshl_add_u64 v[14:15], v[12:13], 0, v[2:3]
	v_lshlrev_b32_e32 v2, 11, v1
	s_waitcnt lgkmcnt(1)
	global_store_dwordx4 v[14:15], v[4:7], off sc1
	s_nop 1
	v_lshl_add_u64 v[4:5], v[12:13], 0, v[2:3]
	s_waitcnt lgkmcnt(0)
	global_store_dwordx4 v[4:5], v[8:11], off sc1
	s_waitcnt lgkmcnt(0)
	s_barrier
	s_lshl_b32 s3, s2, 3
	s_and_b32 s3, s3, 56
	s_ashr_i32 s17, s2, 5
	s_add_i32 s20, s3, s17
	s_ashr_i32 s21, s20, 31
	s_bfe_u32 s16, s2, 0x20003
	s_lshl_b64 s[4:5], s[20:21], 17
	s_lshl_b64 s[6:7], s[20:21], 19
	s_add_u32 s6, s12, s6
	s_addc_u32 s7, s13, s7
	s_lshl_b32 s3, s16, 19
	s_add_u32 s3, s14, s3
	v_ashrrev_i32_e32 v2, 6, v0
	v_lshlrev_b32_e32 v1, 4, v0
	s_addc_u32 s13, s15, 0
	v_lshlrev_b32_e32 v4, 9, v2
	v_and_b32_e32 v5, 0x1f0, v1
	s_add_u32 s12, s3, 0x400000
	v_and_or_b32 v32, v4, s0, v5
	v_lshlrev_b32_e32 v4, 5, v2
	v_and_b32_e32 v5, 48, v1
	s_addc_u32 s13, s13, 0
	v_bitop3_b32 v4, v4, v5, 32 bitop3:0x6c
	s_and_b32 s15, s2, 8
	s_add_i32 s3, s20, 3
	v_bfe_u32 v31, v0, 5, 1
	v_lshrrev_b32_e32 v34, 1, v4
	v_add_u32_e32 v4, s15, v2
	s_mov_b32 s20, 0x3ffffe
	v_and_or_b32 v30, v4, s20, v31
	v_bfe_i32 v5, v30, 0, 22
	v_bfe_u32 v4, v30, 21, 1
	v_add_u32_e32 v6, v5, v4
	v_lshlrev_b32_e32 v4, 3, v6
	v_and_b32_e32 v6, 0x7fffffe, v6
	s_lshl_b32 s0, s17, 4
	v_sub_u32_e32 v5, v5, v6
	s_and_b32 s17, s0, 16
	v_lshl_or_b32 v6, v5, 5, v34
	v_add_u32_e32 v5, s17, v2
	v_and_or_b32 v35, v5, s20, v31
	v_bfe_i32 v7, v35, 0, 22
	v_bfe_u32 v8, v35, 21, 1
	v_add_u32_e32 v8, v7, v8
	v_lshlrev_b32_e32 v9, 3, v8
	v_and_b32_e32 v8, 0x7fffffe, v8
	v_add_u32_e32 v5, 8, v5
	v_sub_u32_e32 v7, v7, v8
	v_and_or_b32 v36, v5, s20, v31
	v_lshl_or_b32 v98, v7, 5, v34
	v_bfe_i32 v5, v36, 0, 22
	v_bfe_u32 v7, v36, 21, 1
	v_add_u32_e32 v7, v5, v7
	v_lshrrev_b32_e32 v33, 6, v32
	v_lshlrev_b32_e32 v8, 3, v7
	v_and_b32_e32 v7, 0x7fffffe, v7
	s_and_b32 s3, s3, 15
	v_and_or_b32 v4, v4, -16, v33
	v_sub_u32_e32 v5, v5, v7
	v_and_or_b32 v14, v9, -16, v33
	v_lshl_or_b32 v100, v5, 5, v34
	v_ashrrev_i32_e32 v5, 31, v4
	s_lshl_b32 s14, s3, 6
	s_lshl_b32 s0, s3, 8
	s_lshl_b32 s2, s3, 7
	v_and_or_b32 v16, v8, -16, v33
	v_lshlrev_b64 v[4:5], 12, v[4:5]
	s_add_u32 s2, s12, s2
	v_ashrrev_i32_e32 v15, 31, v14
	v_lshl_add_u64 v[4:5], s[6:7], 0, v[4:5]
	v_ashrrev_i32_e32 v7, 31, v6
	s_addc_u32 s3, s13, 0
	v_lshlrev_b64 v[102:103], 11, v[14:15]
	v_ashrrev_i32_e32 v99, 31, v98
	v_ashrrev_i32_e32 v17, 31, v16
	v_lshl_add_u64 v[8:9], v[4:5], 0, s[0:1]
	v_lshlrev_b64 v[38:39], 2, v[6:7]
	v_lshl_add_u64 v[14:15], s[2:3], 0, v[102:103]
	v_lshlrev_b64 v[22:23], 1, v[98:99]
	v_lshlrev_b64 v[104:105], 11, v[16:17]
	v_ashrrev_i32_e32 v101, 31, v100
	v_lshl_add_u64 v[18:19], v[8:9], 0, v[38:39]
	v_lshl_add_u64 v[24:25], v[14:15], 0, v[22:23]
	v_lshl_add_u64 v[14:15], s[2:3], 0, v[104:105]
	v_lshlrev_b64 v[26:27], 1, v[100:101]
	global_load_dwordx4 v[6:9], v[18:19], off offset:16
	global_load_dwordx4 v[10:13], v[18:19], off
	v_lshl_add_u64 v[28:29], v[14:15], 0, v[26:27]
	global_load_dwordx4 v[14:17], v[24:25], off
	global_load_dwordx4 v[18:21], v[28:29], off
	v_lshlrev_b32_e32 v24, 10, v30
	v_or_b32_e32 v125, v24, v32
	v_xad_u32 v24, s15, 8, v2
	v_and_or_b32 v24, v24, s20, v31
	v_lshlrev_b32_e32 v25, 10, v24
	v_or_b32_e32 v122, v25, v32
	v_bfe_i32 v25, v24, 0, 22
	v_bfe_u32 v24, v24, 21, 1
	v_add_u32_e32 v28, v25, v24
	v_lshlrev_b32_e32 v24, 3, v28
	v_and_b32_e32 v28, 0x7fffffe, v28
	v_sub_u32_e32 v25, v25, v28
	v_lshl_or_b32 v28, v25, 5, v34
	v_lshlrev_b32_e32 v25, 10, v35
	v_or_b32_e32 v126, v25, v32
	v_lshlrev_b32_e32 v25, 10, v36
	v_or_b32_e32 v127, v25, v32
	v_xad_u32 v25, s17, 16, v2
	v_and_or_b32 v25, v25, s20, v31
	v_lshlrev_b32_e32 v29, 10, v25
	v_or_b32_e32 v123, v29, v32
	v_bfe_i32 v29, v25, 0, 22
	v_bfe_u32 v25, v25, 21, 1
	v_add_u32_e32 v25, v29, v25
	v_and_b32_e32 v121, 3, v2
	v_lshlrev_b32_e32 v30, 3, v25
	v_and_b32_e32 v25, 0x7fffffe, v25
	v_xad_u32 v2, s17, 24, v2
	v_sub_u32_e32 v25, v29, v25
	v_and_or_b32 v2, v2, s20, v31
	v_lshl_or_b32 v106, v25, 5, v34
	v_lshlrev_b32_e32 v25, 10, v2
	v_or_b32_e32 v124, v25, v32
	v_bfe_i32 v25, v2, 0, 22
	v_bfe_u32 v2, v2, 21, 1
	v_add_u32_e32 v2, v25, v2
	v_lshlrev_b32_e32 v29, 3, v2
	v_and_b32_e32 v2, 0x7fffffe, v2
	v_and_b32_e32 v118, 15, v0
	v_sub_u32_e32 v2, v25, v2
	v_lshlrev_b32_e32 v25, 2, v0
	v_ashrrev_i32_e32 v120, 8, v0
	v_and_or_b32 v32, v29, -16, v33
	v_lshl_or_b32 v108, v2, 5, v34
	v_and_b32_e32 v2, 48, v0
	v_and_b32_e32 v25, 32, v25
	v_lshlrev_b32_e32 v29, 6, v118
	v_and_b32_e32 v119, 63, v0
	v_and_or_b32 v24, v24, -16, v33
	v_and_or_b32 v30, v30, -16, v33
	v_lshlrev_b32_e32 v68, 13, v120
	v_bitop3_b32 v2, v29, v25, v2 bitop3:0x36
	v_ashrrev_i32_e32 v25, 31, v24
	v_lshlrev_b64 v[24:25], 12, v[24:25]
	v_lshl_add_u64 v[56:57], s[6:7], 0, v[24:25]
	v_ashrrev_i32_e32 v29, 31, v28
	v_lshl_add_u64 v[24:25], v[56:57], 0, s[0:1]
	v_lshlrev_b64 v[58:59], 2, v[28:29]
	v_ashrrev_i32_e32 v31, 31, v30
	v_lshl_add_u64 v[24:25], v[24:25], 0, v[58:59]
	v_lshlrev_b64 v[110:111], 11, v[30:31]
	v_ashrrev_i32_e32 v107, 31, v106
	v_ashrrev_i32_e32 v33, 31, v32
	global_load_dwordx4 v[40:43], v[24:25], off offset:16
	global_load_dwordx4 v[44:47], v[24:25], off
	v_lshl_add_u64 v[24:25], s[2:3], 0, v[110:111]
	v_lshlrev_b64 v[60:61], 1, v[106:107]
	v_lshlrev_b64 v[112:113], 11, v[32:33]
	v_ashrrev_i32_e32 v109, 31, v108
	v_lshl_add_u64 v[24:25], v[24:25], 0, v[60:61]
	v_lshl_add_u64 v[28:29], s[2:3], 0, v[112:113]
	v_lshlrev_b64 v[62:63], 1, v[108:109]
	v_lshl_add_u64 v[28:29], v[28:29], 0, v[62:63]
	global_load_dwordx4 v[48:51], v[24:25], off
	global_load_dwordx4 v[52:55], v[28:29], off
	s_add_i32 s0, s14, 64
	s_and_b32 s2, s0, 0x3c0
	s_lshl_b32 s0, s2, 2
	s_lshl_b32 s2, s2, 1
	v_lshl_add_u64 v[24:25], v[4:5], 0, s[0:1]
	s_add_u32 s2, s12, s2
	v_lshl_add_u64 v[24:25], v[24:25], 0, v[38:39]
	s_addc_u32 s3, s13, 0
	global_load_dwordx4 v[30:33], v[24:25], off offset:16
	global_load_dwordx4 v[34:37], v[24:25], off
	v_lshl_add_u64 v[24:25], s[2:3], 0, v[102:103]
	v_lshl_add_u64 v[64:65], v[24:25], 0, v[22:23]
	v_lshl_add_u64 v[22:23], s[2:3], 0, v[104:105]
	v_lshl_add_u64 v[66:67], v[22:23], 0, v[26:27]
	global_load_dwordx4 v[26:29], v[64:65], off
	global_load_dwordx4 v[22:25], v[66:67], off
	v_add_u32_e32 v64, 0, v125
	s_waitcnt vmcnt(10)
	v_cvt_pk_bf16_f32 v10, v10, v11
	v_cvt_pk_bf16_f32 v11, v12, v13
	v_cvt_pk_bf16_f32 v12, v6, v7
	v_add_u32_e32 v6, 0, v126
	v_cvt_pk_bf16_f32 v13, v8, v9
	ds_write_b128 v64, v[10:13]
	s_waitcnt vmcnt(9)
	ds_write_b128 v6, v[14:17] offset:32768
	v_add_u32_e32 v6, 0, v127
	s_waitcnt vmcnt(8)
	ds_write_b128 v6, v[18:21] offset:32768
	v_add_u32_e32 v10, 0, v122
	s_waitcnt vmcnt(6)
	v_cvt_pk_bf16_f32 v6, v44, v45
	v_cvt_pk_bf16_f32 v7, v46, v47
	v_cvt_pk_bf16_f32 v8, v40, v41
	v_cvt_pk_bf16_f32 v9, v42, v43
	ds_write_b128 v10, v[6:9]
	v_add_u32_e32 v6, 0, v123
	s_waitcnt vmcnt(5)
	ds_write_b128 v6, v[48:51] offset:32768
	v_add_u32_e32 v6, 0, v124
	s_waitcnt vmcnt(4)
	ds_write_b128 v6, v[52:55] offset:32768
	v_lshl_add_u64 v[6:7], v[56:57], 0, s[0:1]
	v_lshl_add_u64 v[14:15], v[6:7], 0, v[58:59]
	global_load_dwordx4 v[6:9], v[14:15], off offset:16
	global_load_dwordx4 v[10:13], v[14:15], off
	v_lshl_add_u64 v[14:15], s[2:3], 0, v[110:111]
	v_lshl_add_u64 v[40:41], v[14:15], 0, v[60:61]
	v_lshl_add_u64 v[14:15], s[2:3], 0, v[112:113]
	v_lshl_add_u64 v[42:43], v[14:15], 0, v[62:63]
	global_load_dwordx4 v[18:21], v[40:41], off
	global_load_dwordx4 v[14:17], v[42:43], off
	v_lshlrev_b32_e32 v40, 13, v121
	s_cmp_lg_u32 0, -1
	s_waitcnt lgkmcnt(0)
	s_cselect_b32 s0, 0, 0
	v_add3_u32 v128, v68, s0, v2
	s_add_i32 s0, s0, 0x8000
	v_add3_u32 v129, v40, s0, v2
	v_lshl_add_u64 v[114:115], v[4:5], 0, v[38:39]
	v_lshl_add_u64 v[116:117], v[56:57], 0, v[58:59]
	s_add_i32 s2, s14, 0x80
	s_mov_b32 s3, 0
	v_mov_b32_e32 v2, v3
	v_mov_b32_e32 v4, v3
	v_mov_b32_e32 v5, v3
	v_mov_b32_e32 v38, v3
	v_mov_b32_e32 v39, v3
	v_mov_b32_e32 v40, v3
	v_mov_b32_e32 v41, v3
	v_mov_b32_e32 v42, v3
	v_mov_b32_e32 v43, v3
	v_mov_b32_e32 v44, v3
	v_mov_b32_e32 v45, v3
	v_mov_b32_e32 v46, v3
	v_mov_b32_e32 v47, v3
	v_mov_b32_e32 v48, v3
	v_mov_b32_e32 v49, v3
	v_mov_b32_e32 v50, v3
	v_mov_b32_e32 v51, v3
	v_mov_b32_e32 v52, v3
	v_mov_b32_e32 v53, v3
	v_mov_b32_e32 v54, v3
	v_mov_b32_e32 v55, v3
	v_mov_b32_e32 v56, v3
	v_mov_b32_e32 v57, v3
	v_mov_b32_e32 v58, v3
	v_mov_b32_e32 v59, v3
	v_mov_b32_e32 v60, v3
	v_mov_b32_e32 v61, v3
	v_mov_b32_e32 v62, v3
	v_mov_b32_e32 v63, v3
	v_mov_b32_e32 v64, v3
	v_mov_b32_e32 v65, v3
	v_mov_b32_e32 v66, v3
	v_mov_b32_e32 v67, v3
	v_mov_b32_e32 v68, v3
	v_mov_b32_e32 v69, v3
	v_mov_b32_e32 v70, v3
	v_mov_b32_e32 v71, v3
	v_mov_b32_e32 v72, v3
	v_mov_b32_e32 v73, v3
	v_mov_b32_e32 v74, v3
	v_mov_b32_e32 v75, v3
	v_mov_b32_e32 v76, v3
	v_mov_b32_e32 v77, v3
	v_mov_b32_e32 v78, v3
	v_mov_b32_e32 v79, v3
	v_mov_b32_e32 v80, v3
	v_mov_b32_e32 v81, v3
	v_mov_b32_e32 v82, v3
	v_mov_b32_e32 v83, v3
	v_mov_b32_e32 v84, v3
	v_mov_b32_e32 v85, v3
	v_mov_b32_e32 v86, v3
	v_mov_b32_e32 v87, v3
	v_mov_b32_e32 v88, v3
	v_mov_b32_e32 v89, v3
	v_mov_b32_e32 v90, v3
	v_mov_b32_e32 v91, v3
	v_mov_b32_e32 v92, v3
	v_mov_b32_e32 v93, v3
	v_mov_b32_e32 v94, v3
	v_mov_b32_e32 v95, v3
	v_mov_b32_e32 v96, v3
	v_mov_b32_e32 v97, v3
	s_and_b32 s0, s3, 0x10000
	v_add_u32_e32 v158, s0, v128
	v_add_u32_e32 v159, s0, v129
	s_barrier
.LBB1_3:
	ds_read_b128 v[130:133], v159 offset:0
	ds_read_b128 v[134:137], v159 offset:0x800
	ds_read_b128 v[138:141], v159 offset:0x1000
	ds_read_b128 v[142:145], v159 offset:0x1800
	ds_read_b128 v[146:149], v158 offset:0
	ds_read_b128 v[150:153], v158 offset:0x800
	ds_read_b128 v[154:157], v158 offset:0x1000
	s_waitcnt lgkmcnt(2)
	v_mfma_f32_16x16x32_bf16 v[94:97], v[130:133], v[146:149], v[94:97]
	v_mfma_f32_16x16x32_bf16 v[90:93], v[134:137], v[146:149], v[90:93]
	v_mfma_f32_16x16x32_bf16 v[86:89], v[138:141], v[146:149], v[86:89]
	v_mfma_f32_16x16x32_bf16 v[82:85], v[142:145], v[146:149], v[82:85]
	ds_read_b128 v[146:149], v158 offset:0x1800
	s_waitcnt lgkmcnt(2)
	v_mfma_f32_16x16x32_bf16 v[78:81], v[130:133], v[150:153], v[78:81]
	v_mfma_f32_16x16x32_bf16 v[74:77], v[134:137], v[150:153], v[74:77]
	v_mfma_f32_16x16x32_bf16 v[70:73], v[138:141], v[150:153], v[70:73]
	v_mfma_f32_16x16x32_bf16 v[66:69], v[142:145], v[150:153], v[66:69]
	s_waitcnt lgkmcnt(0)
	v_mfma_f32_16x16x32_bf16 v[62:65], v[130:133], v[154:157], v[62:65]
	v_mfma_f32_16x16x32_bf16 v[58:61], v[134:137], v[154:157], v[58:61]
	v_mfma_f32_16x16x32_bf16 v[54:57], v[138:141], v[154:157], v[54:57]
	v_mfma_f32_16x16x32_bf16 v[50:53], v[142:145], v[154:157], v[50:53]
	v_mfma_f32_16x16x32_bf16 v[46:49], v[130:133], v[146:149], v[46:49]
	v_mfma_f32_16x16x32_bf16 v[42:45], v[134:137], v[146:149], v[42:45]
	v_mfma_f32_16x16x32_bf16 v[38:41], v[138:141], v[146:149], v[38:41]
	v_mfma_f32_16x16x32_bf16 v[2:5], v[142:145], v[146:149], v[2:5]
	s_xor_b32 s0, s0, 0x10000
	s_and_b32 s6, s2, 0x3c0
	s_add_i32 s14, s0, 0
	s_lshl_b32 s0, s6, 2
	s_lshl_b32 s6, s6, 1
	s_add_u32 s6, s12, s6
	s_waitcnt vmcnt(6)
	v_cvt_pk_bf16_f32 v34, v34, v35
	v_cvt_pk_bf16_f32 v35, v36, v37
	v_cvt_pk_bf16_f32 v36, v30, v31
	v_cvt_pk_bf16_f32 v37, v32, v33
	v_add_u32_e32 v30, s14, v125
	s_addc_u32 s7, s13, 0
	v_add_u32_e32 v31, s14, v126
	v_add_u32_e32 v32, s14, v127
	ds_write_b128 v30, v[34:37]
	s_waitcnt vmcnt(5)
	ds_write_b128 v31, v[26:29] offset:32768
	s_waitcnt vmcnt(4)
	ds_write_b128 v32, v[22:25] offset:32768
	v_lshl_add_u64 v[22:23], s[6:7], 0, v[102:103]
	v_lshl_add_u64 v[24:25], s[6:7], 0, v[104:105]
	v_lshl_add_u64 v[130:131], v[114:115], 0, s[0:1]
	v_lshl_add_u64 v[22:23], v[98:99], 1, v[22:23]
	v_lshl_add_u64 v[24:25], v[100:101], 1, v[24:25]
	global_load_dwordx4 v[30:33], v[130:131], off offset:16
	global_load_dwordx4 v[34:37], v[130:131], off
	global_load_dwordx4 v[26:29], v[22:23], off
	s_nop 0
	global_load_dwordx4 v[22:25], v[24:25], off
	ds_read_b128 v[130:133], v159 offset:0x400
	ds_read_b128 v[134:137], v159 offset:0xc00
	ds_read_b128 v[138:141], v159 offset:0x1400
	ds_read_b128 v[142:145], v159 offset:0x1c00
	ds_read_b128 v[146:149], v158 offset:0x400
	ds_read_b128 v[150:153], v158 offset:0xc00
	ds_read_b128 v[154:157], v158 offset:0x1400
	s_waitcnt lgkmcnt(2)
	v_mfma_f32_16x16x32_bf16 v[94:97], v[130:133], v[146:149], v[94:97]
	v_mfma_f32_16x16x32_bf16 v[90:93], v[134:137], v[146:149], v[90:93]
	v_mfma_f32_16x16x32_bf16 v[86:89], v[138:141], v[146:149], v[86:89]
	v_mfma_f32_16x16x32_bf16 v[82:85], v[142:145], v[146:149], v[82:85]
	ds_read_b128 v[146:149], v158 offset:0x1c00
	s_waitcnt lgkmcnt(2)
	v_mfma_f32_16x16x32_bf16 v[78:81], v[130:133], v[150:153], v[78:81]
	v_mfma_f32_16x16x32_bf16 v[74:77], v[134:137], v[150:153], v[74:77]
	v_mfma_f32_16x16x32_bf16 v[70:73], v[138:141], v[150:153], v[70:73]
	v_mfma_f32_16x16x32_bf16 v[66:69], v[142:145], v[150:153], v[66:69]
	s_waitcnt lgkmcnt(0)
	v_mfma_f32_16x16x32_bf16 v[62:65], v[130:133], v[154:157], v[62:65]
	v_mfma_f32_16x16x32_bf16 v[58:61], v[134:137], v[154:157], v[58:61]
	v_mfma_f32_16x16x32_bf16 v[54:57], v[138:141], v[154:157], v[54:57]
	v_mfma_f32_16x16x32_bf16 v[50:53], v[142:145], v[154:157], v[50:53]
	v_mfma_f32_16x16x32_bf16 v[46:49], v[130:133], v[146:149], v[46:49]
	v_mfma_f32_16x16x32_bf16 v[42:45], v[134:137], v[146:149], v[42:45]
	v_mfma_f32_16x16x32_bf16 v[38:41], v[138:141], v[146:149], v[38:41]
	v_mfma_f32_16x16x32_bf16 v[2:5], v[142:145], v[146:149], v[2:5]
	v_add_u32_e32 v130, s14, v122
	s_waitcnt vmcnt(6)
	v_cvt_pk_bf16_f32 v10, v10, v11
	v_cvt_pk_bf16_f32 v11, v12, v13
	v_cvt_pk_bf16_f32 v12, v6, v7
	v_add_u32_e32 v6, s14, v123
	v_cvt_pk_bf16_f32 v13, v8, v9
	ds_write_b128 v130, v[10:13]
	s_waitcnt vmcnt(5)
	ds_write_b128 v6, v[18:21] offset:32768
	v_add_u32_e32 v6, s14, v124
	s_waitcnt vmcnt(4)
	ds_write_b128 v6, v[14:17] offset:32768
	v_lshl_add_u64 v[14:15], s[6:7], 0, v[110:111]
	v_lshl_add_u64 v[16:17], s[6:7], 0, v[112:113]
	v_lshl_add_u64 v[10:11], v[116:117], 0, s[0:1]
	v_lshl_add_u64 v[14:15], v[106:107], 1, v[14:15]
	v_lshl_add_u64 v[16:17], v[108:109], 1, v[16:17]
	global_load_dwordx4 v[6:9], v[10:11], off offset:16
	s_nop 0
	global_load_dwordx4 v[10:13], v[10:11], off
	s_nop 0
	global_load_dwordx4 v[18:21], v[14:15], off
	s_nop 0
	global_load_dwordx4 v[14:17], v[16:17], off
	s_waitcnt lgkmcnt(0)
	s_add_i32 s2, s2, 64
	s_add_i32 s3, s3, 0x10000
	s_and_b32 s0, s3, 0x10000
	v_add_u32_e32 v158, s0, v128
	v_add_u32_e32 v159, s0, v129
	s_cmp_lg_u32 s3, 0xe0000
	s_barrier
	s_cbranch_scc1 .LBB1_3
	ds_read_b128 v[98:101], v129 offset:0
	ds_read_b128 v[102:105], v129 offset:0x800
	ds_read_b128 v[106:109], v129 offset:0x1000
	ds_read_b128 v[110:113], v129 offset:0x1800
	ds_read_b128 v[114:117], v128 offset:0
	ds_read_b128 v[130:133], v128 offset:0x800
	ds_read_b128 v[134:137], v128 offset:0x1000
	s_nop 0
	s_waitcnt lgkmcnt(2)
	s_nop 0
	v_mfma_f32_16x16x32_bf16 v[94:97], v[98:101], v[114:117], v[94:97]
	v_mfma_f32_16x16x32_bf16 v[90:93], v[102:105], v[114:117], v[90:93]
	v_mfma_f32_16x16x32_bf16 v[86:89], v[106:109], v[114:117], v[86:89]
	v_mfma_f32_16x16x32_bf16 v[82:85], v[110:113], v[114:117], v[82:85]
	ds_read_b128 v[114:117], v128 offset:0x1800
	s_waitcnt lgkmcnt(2)
	s_nop 0
	v_mfma_f32_16x16x32_bf16 v[78:81], v[98:101], v[130:133], v[78:81]
	v_mfma_f32_16x16x32_bf16 v[74:77], v[102:105], v[130:133], v[74:77]
	v_mfma_f32_16x16x32_bf16 v[70:73], v[106:109], v[130:133], v[70:73]
	v_mfma_f32_16x16x32_bf16 v[66:69], v[110:113], v[130:133], v[66:69]
	s_waitcnt lgkmcnt(1)
	s_nop 0
	v_mfma_f32_16x16x32_bf16 v[62:65], v[98:101], v[134:137], v[62:65]
	v_mfma_f32_16x16x32_bf16 v[58:61], v[102:105], v[134:137], v[58:61]
	v_mfma_f32_16x16x32_bf16 v[54:57], v[106:109], v[134:137], v[54:57]
	v_mfma_f32_16x16x32_bf16 v[50:53], v[110:113], v[134:137], v[50:53]
	s_waitcnt lgkmcnt(0)
	s_nop 0
	v_mfma_f32_16x16x32_bf16 v[46:49], v[98:101], v[114:117], v[46:49]
	v_mfma_f32_16x16x32_bf16 v[42:45], v[102:105], v[114:117], v[42:45]
	v_mfma_f32_16x16x32_bf16 v[38:41], v[106:109], v[114:117], v[38:41]
	v_mfma_f32_16x16x32_bf16 v[2:5], v[110:113], v[114:117], v[2:5]
	v_add_u32_e32 v98, s18, v125
	s_waitcnt vmcnt(6)
	v_cvt_pk_bf16_f32 v34, v34, v35
	v_cvt_pk_bf16_f32 v35, v36, v37
	v_cvt_pk_bf16_f32 v36, v30, v31
	v_add_u32_e32 v30, s19, v126
	v_cvt_pk_bf16_f32 v37, v32, v33
	ds_write_b128 v98, v[34:37]
	s_waitcnt vmcnt(5)
	ds_write_b128 v30, v[26:29]
	v_add_u32_e32 v26, s19, v127
	s_waitcnt vmcnt(4)
	ds_write_b128 v26, v[22:25]
	ds_read_b128 v[22:25], v129 offset:0x400
	ds_read_b128 v[26:29], v129 offset:0xc00
	ds_read_b128 v[30:33], v129 offset:0x1400
	ds_read_b128 v[34:37], v129 offset:0x1c00
	ds_read_b128 v[98:101], v128 offset:0x400
	ds_read_b128 v[102:105], v128 offset:0xc00
	ds_read_b128 v[106:109], v128 offset:0x1400
	s_nop 0
	s_waitcnt lgkmcnt(2)
	s_nop 0
	v_mfma_f32_16x16x32_bf16 v[94:97], v[22:25], v[98:101], v[94:97]
	v_mfma_f32_16x16x32_bf16 v[90:93], v[26:29], v[98:101], v[90:93]
	v_mfma_f32_16x16x32_bf16 v[86:89], v[30:33], v[98:101], v[86:89]
	v_mfma_f32_16x16x32_bf16 v[82:85], v[34:37], v[98:101], v[82:85]
	ds_read_b128 v[98:101], v128 offset:0x1c00
	s_waitcnt lgkmcnt(2)
	s_nop 0
	v_mfma_f32_16x16x32_bf16 v[78:81], v[22:25], v[102:105], v[78:81]
	v_mfma_f32_16x16x32_bf16 v[74:77], v[26:29], v[102:105], v[74:77]
	v_mfma_f32_16x16x32_bf16 v[70:73], v[30:33], v[102:105], v[70:73]
	v_mfma_f32_16x16x32_bf16 v[66:69], v[34:37], v[102:105], v[66:69]
	s_waitcnt lgkmcnt(1)
	s_nop 0
	v_mfma_f32_16x16x32_bf16 v[62:65], v[22:25], v[106:109], v[62:65]
	v_mfma_f32_16x16x32_bf16 v[58:61], v[26:29], v[106:109], v[58:61]
	v_mfma_f32_16x16x32_bf16 v[54:57], v[30:33], v[106:109], v[54:57]
	v_mfma_f32_16x16x32_bf16 v[50:53], v[34:37], v[106:109], v[50:53]
	s_waitcnt lgkmcnt(0)
	s_nop 0
	v_mfma_f32_16x16x32_bf16 v[22:25], v[22:25], v[98:101], v[46:49]
	v_mfma_f32_16x16x32_bf16 v[26:29], v[26:29], v[98:101], v[42:45]
	v_mfma_f32_16x16x32_bf16 v[30:33], v[30:33], v[98:101], v[38:41]
	v_mfma_f32_16x16x32_bf16 v[2:5], v[34:37], v[98:101], v[2:5]
	v_add_u32_e32 v34, s18, v122
	s_waitcnt vmcnt(2)
	v_cvt_pk_bf16_f32 v10, v10, v11
	v_cvt_pk_bf16_f32 v11, v12, v13
	v_cvt_pk_bf16_f32 v12, v6, v7
	v_add_u32_e32 v6, s19, v123
	s_lshl_b64 s[0:1], s[4:5], 1
	v_cvt_pk_bf16_f32 v13, v8, v9
	ds_write_b128 v34, v[10:13]
	s_waitcnt vmcnt(1)
	ds_write_b128 v6, v[18:21]
	v_add_u32_e32 v6, s19, v124
	s_add_u32 s0, s10, s0
	s_waitcnt vmcnt(0)
	ds_write_b128 v6, v[14:17]
	s_addc_u32 s1, s11, s1
	s_lshl_b32 s2, s16, 9
	s_waitcnt lgkmcnt(0)
	s_barrier
	v_add_u32_e32 v110, 0x10000, v128
	v_add_u32_e32 v102, 0x10000, v129
	ds_read_b128 v[6:9], v102 offset:0
	ds_read_b128 v[10:13], v102 offset:0x800
	ds_read_b128 v[14:17], v102 offset:0x1000
	ds_read_b128 v[18:21], v102 offset:0x1800
	ds_read_b128 v[34:37], v110 offset:0
	ds_read_b128 v[38:41], v110 offset:0x800
	ds_read_b128 v[42:45], v110 offset:0x1000
	s_add_u32 s0, s0, s2
	s_addc_u32 s1, s1, 0
	s_lshl_b32 s2, s16, 10
	s_waitcnt lgkmcnt(2)
	s_add_u32 s2, s8, s2
	v_mfma_f32_16x16x32_bf16 v[46:49], v[6:9], v[34:37], v[94:97]
	s_addc_u32 s3, s9, 0
	v_mfma_f32_16x16x32_bf16 v[90:93], v[10:13], v[34:37], v[90:93]
	v_mfma_f32_16x16x32_bf16 v[86:89], v[14:17], v[34:37], v[86:89]
	v_mfma_f32_16x16x32_bf16 v[34:37], v[18:21], v[34:37], v[82:85]
	ds_read_b128 v[82:85], v110 offset:0x1800
	s_waitcnt lgkmcnt(2)
	s_nop 0
	v_mfma_f32_16x16x32_bf16 v[78:81], v[6:9], v[38:41], v[78:81]
	v_mfma_f32_16x16x32_bf16 v[74:77], v[10:13], v[38:41], v[74:77]
	v_mfma_f32_16x16x32_bf16 v[70:73], v[14:17], v[38:41], v[70:73]
	v_mfma_f32_16x16x32_bf16 v[38:41], v[18:21], v[38:41], v[66:69]
	s_waitcnt lgkmcnt(1)
	s_nop 0
	v_mfma_f32_16x16x32_bf16 v[62:65], v[6:9], v[42:45], v[62:65]
	v_mfma_f32_16x16x32_bf16 v[58:61], v[10:13], v[42:45], v[58:61]
	v_mfma_f32_16x16x32_bf16 v[54:57], v[14:17], v[42:45], v[54:57]
	v_mfma_f32_16x16x32_bf16 v[42:45], v[18:21], v[42:45], v[50:53]
	s_waitcnt lgkmcnt(0)
	s_nop 0
	v_mfma_f32_16x16x32_bf16 v[50:53], v[6:9], v[82:85], v[22:25]
	v_mfma_f32_16x16x32_bf16 v[66:69], v[10:13], v[82:85], v[26:29]
	v_mfma_f32_16x16x32_bf16 v[94:97], v[14:17], v[82:85], v[30:33]
	v_mfma_f32_16x16x32_bf16 v[2:5], v[18:21], v[82:85], v[2:5]
	ds_read_b128 v[18:21], v102 offset:0x400
	ds_read_b128 v[82:85], v102 offset:0xc00
	ds_read_b128 v[98:101], v102 offset:0x1400
	ds_read_b128 v[102:105], v102 offset:0x1c00
	ds_read_b128 v[6:9], v110 offset:0x400
	ds_read_b128 v[10:13], v110 offset:0xc00
	ds_read_b128 v[106:109], v110 offset:0x1400
	s_nop 0
	s_waitcnt lgkmcnt(2)
	s_nop 0
	v_mfma_f32_16x16x32_bf16 v[46:49], v[18:21], v[6:9], v[46:49]
	v_mfma_f32_16x16x32_bf16 v[90:93], v[82:85], v[6:9], v[90:93]
	v_mfma_f32_16x16x32_bf16 v[30:33], v[98:101], v[6:9], v[86:89]
	v_mfma_f32_16x16x32_bf16 v[14:17], v[102:105], v[6:9], v[34:37]
	ds_read_b128 v[86:89], v110 offset:0x1c00
	s_waitcnt lgkmcnt(2)
	s_nop 0
	v_mfma_f32_16x16x32_bf16 v[78:81], v[18:21], v[10:13], v[78:81]
	v_mfma_f32_16x16x32_bf16 v[74:77], v[82:85], v[10:13], v[74:77]
	v_mfma_f32_16x16x32_bf16 v[26:29], v[98:101], v[10:13], v[70:73]
	v_mfma_f32_16x16x32_bf16 v[10:13], v[102:105], v[10:13], v[38:41]
	s_waitcnt lgkmcnt(1)
	s_nop 0
	v_mfma_f32_16x16x32_bf16 v[62:65], v[18:21], v[106:109], v[62:65]
	v_mfma_f32_16x16x32_bf16 v[38:41], v[82:85], v[106:109], v[58:61]
	v_mfma_f32_16x16x32_bf16 v[22:25], v[98:101], v[106:109], v[54:57]
	v_mfma_f32_16x16x32_bf16 v[6:9], v[102:105], v[106:109], v[42:45]
	s_waitcnt lgkmcnt(0)
	s_nop 0
	v_mfma_f32_16x16x32_bf16 v[42:45], v[18:21], v[86:89], v[50:53]
	v_mfma_f32_16x16x32_bf16 v[34:37], v[82:85], v[86:89], v[66:69]
	v_mfma_f32_16x16x32_bf16 v[18:21], v[98:101], v[86:89], v[94:97]
	v_mfma_f32_16x16x32_bf16 v[2:5], v[102:105], v[86:89], v[2:5]
	v_lshrrev_b32_e32 v50, 2, v119
	v_and_b32_e32 v50, 12, v50
	v_lshl_or_b32 v66, v121, 6, v50
	v_lshlrev_b32_e32 v67, 2, v66
	s_waitcnt lgkmcnt(0)
	s_barrier
	global_load_dwordx4 v[50:53], v67, s[2:3]
	global_load_dwordx4 v[54:57], v67, s[2:3] offset:64
	v_lshrrev_b32_e32 v58, 1, v119
	v_lshl_or_b32 v59, v120, 6, v118
	v_and_b32_e32 v68, 8, v58
	v_lshl_add_u32 v69, v59, 9, 0
	v_or_b32_e32 v70, 16, v59
	v_or_b32_e32 v71, 48, v59
	v_lshrrev_b32_e32 v58, 3, v66
	v_or_b32_e32 v59, 16, v66
	v_bitop3_b32 v83, v70, v58, 31 bitop3:0x6c
	v_lshrrev_b32_e32 v85, 3, v59
	v_lshl_add_u32 v72, v70, 9, 0
	v_xor_b32_e32 v82, v58, v118
	v_bitop3_b32 v84, v71, v58, 31 bitop3:0x6c
	v_lshlrev_b32_e32 v83, 4, v83
	v_xor_b32_e32 v86, v85, v118
	v_lshl_add_u32 v73, v71, 9, 0
	v_lshlrev_b32_e32 v82, 4, v82
	v_lshlrev_b32_e32 v84, 4, v84
	v_add3_u32 v83, v72, v83, v68
	v_lshlrev_b32_e32 v86, 4, v86
	global_load_dwordx4 v[58:61], v67, s[2:3] offset:128
	v_add3_u32 v82, v69, v82, v68
	v_add3_u32 v84, v73, v84, v68
	v_add3_u32 v86, v69, v86, v68
	s_waitcnt vmcnt(2)
	v_add_f32_e32 v46, v46, v50
	v_add_f32_e32 v47, v47, v51
	v_add_f32_e32 v48, v48, v52
	v_add_f32_e32 v49, v49, v53
	v_add_f32_e32 v78, v78, v50
	v_add_f32_e32 v79, v79, v51
	v_add_f32_e32 v80, v80, v52
	v_add_f32_e32 v81, v81, v53
	v_add_f32_e32 v62, v62, v50
	v_add_f32_e32 v63, v63, v51
	v_add_f32_e32 v42, v42, v50
	v_add_f32_e32 v43, v43, v51
	v_add_f32_e32 v44, v44, v52
	v_add_f32_e32 v45, v45, v53
	s_waitcnt vmcnt(1)
	v_add_f32_e32 v50, v90, v54
	v_add_f32_e32 v51, v91, v55
	v_add_f32_e32 v64, v64, v52
	v_add_f32_e32 v65, v65, v53
	v_add_f32_e32 v52, v92, v56
	v_add_f32_e32 v53, v93, v57
	v_max_f32_e32 v46, 0, v46
	v_max_f32_e32 v47, 0, v47
	v_max_f32_e32 v48, 0, v48
	v_max_f32_e32 v49, 0, v49
	v_max_f32_e32 v78, 0, v78
	v_max_f32_e32 v79, 0, v79
	v_max_f32_e32 v80, 0, v80
	v_max_f32_e32 v81, 0, v81
	v_max_f32_e32 v88, 0, v43
	v_max_f32_e32 v89, 0, v44
	v_max_f32_e32 v90, 0, v45
	v_max_f32_e32 v50, 0, v50
	v_max_f32_e32 v51, 0, v51
	v_cvt_pk_bf16_f32 v43, v48, v49
	v_cvt_pk_bf16_f32 v44, v78, v79
	v_cvt_pk_bf16_f32 v45, v80, v81
	v_max_f32_e32 v62, 0, v62
	v_max_f32_e32 v63, 0, v63
	v_max_f32_e32 v64, 0, v64
	v_max_f32_e32 v65, 0, v65
	v_max_f32_e32 v87, 0, v42
	v_max_f32_e32 v52, 0, v52
	v_max_f32_e32 v53, 0, v53
	v_cvt_pk_bf16_f32 v42, v46, v47
	v_cvt_pk_bf16_f32 v46, v62, v63
	v_cvt_pk_bf16_f32 v47, v64, v65
	v_cvt_pk_bf16_f32 v48, v87, v88
	v_cvt_pk_bf16_f32 v49, v89, v90
	v_cvt_pk_bf16_f32 v50, v50, v51
	v_cvt_pk_bf16_f32 v51, v52, v53
	ds_write_b64 v83, v[44:45]
	ds_write2st64_b64 v82, v[42:43], v[46:47] offset1:32
	ds_write_b64 v84, v[48:49]
	ds_write_b64 v86, v[50:51]
	v_add_f32_e32 v43, v76, v56
	v_add_f32_e32 v44, v77, v57
	v_max_f32_e32 v43, 0, v43
	v_max_f32_e32 v44, 0, v44
	v_add_f32_e32 v42, v75, v55
	v_cvt_pk_bf16_f32 v43, v43, v44
	v_bitop3_b32 v44, v85, v70, 31 bitop3:0x78
	v_add_f32_e32 v74, v74, v54
	v_max_f32_e32 v42, 0, v42
	v_lshlrev_b32_e32 v44, 4, v44
	v_max_f32_e32 v74, 0, v74
	v_cvt_pk_bf16_f32 v42, v74, v42
	v_add3_u32 v44, v72, v44, v68
	ds_write_b64 v44, v[42:43]
	global_load_dwordx4 v[42:45], v67, s[2:3] offset:192
	v_add_f32_e32 v34, v34, v54
	v_add_f32_e32 v35, v35, v55
	v_add_f32_e32 v36, v36, v56
	v_max_f32_e32 v34, 0, v34
	v_max_f32_e32 v35, 0, v35
	v_max_f32_e32 v36, 0, v36
	v_add_f32_e32 v37, v37, v57
	v_max_f32_e32 v37, 0, v37
	v_cvt_pk_bf16_f32 v34, v34, v35
	v_cvt_pk_bf16_f32 v35, v36, v37
	v_bitop3_b32 v36, v85, v71, 31 bitop3:0x78
	v_add_f32_e32 v38, v38, v54
	v_add_f32_e32 v39, v39, v55
	v_lshlrev_b32_e32 v36, 4, v36
	v_max_f32_e32 v38, 0, v38
	v_max_f32_e32 v39, 0, v39
	v_add_f32_e32 v40, v40, v56
	v_add_f32_e32 v41, v41, v57
	v_add3_u32 v36, v73, v36, v68
	v_max_f32_e32 v40, 0, v40
	v_max_f32_e32 v41, 0, v41
	v_cvt_pk_bf16_f32 v38, v38, v39
	v_cvt_pk_bf16_f32 v39, v40, v41
	ds_write_b64 v86, v[38:39] offset:16384
	ds_write_b64 v36, v[34:35]
	v_or_b32_e32 v34, 32, v66
	s_waitcnt vmcnt(1)
	v_add_f32_e32 v30, v30, v58
	v_add_f32_e32 v31, v31, v59
	v_add_f32_e32 v32, v32, v60
	v_add_f32_e32 v26, v26, v58
	v_add_f32_e32 v27, v27, v59
	v_add_f32_e32 v28, v28, v60
	v_add_f32_e32 v18, v18, v58
	v_add_f32_e32 v19, v19, v59
	v_add_f32_e32 v20, v20, v60
	v_lshrrev_b32_e32 v34, 3, v34
	v_max_f32_e32 v30, 0, v30
	v_max_f32_e32 v31, 0, v31
	v_max_f32_e32 v32, 0, v32
	v_add_f32_e32 v33, v33, v61
	v_max_f32_e32 v26, 0, v26
	v_max_f32_e32 v27, 0, v27
	v_max_f32_e32 v28, 0, v28
	v_add_f32_e32 v29, v29, v61
	v_max_f32_e32 v18, 0, v18
	v_max_f32_e32 v19, 0, v19
	v_max_f32_e32 v20, 0, v20
	v_add_f32_e32 v21, v21, v61
	v_max_f32_e32 v33, 0, v33
	v_cvt_pk_bf16_f32 v30, v30, v31
	v_cvt_pk_bf16_f32 v31, v32, v33
	v_xor_b32_e32 v32, v34, v118
	v_max_f32_e32 v29, 0, v29
	v_cvt_pk_bf16_f32 v26, v26, v27
	v_cvt_pk_bf16_f32 v27, v28, v29
	v_bitop3_b32 v28, v34, v70, 31 bitop3:0x78
	v_max_f32_e32 v21, 0, v21
	v_cvt_pk_bf16_f32 v18, v18, v19
	v_cvt_pk_bf16_f32 v19, v20, v21
	v_bitop3_b32 v20, v34, v71, 31 bitop3:0x78
	v_lshlrev_b32_e32 v32, 4, v32
	v_lshlrev_b32_e32 v28, 4, v28
	v_add_f32_e32 v22, v22, v58
	v_add_f32_e32 v23, v23, v59
	v_lshlrev_b32_e32 v20, 4, v20
	v_add3_u32 v32, v69, v32, v68
	v_add3_u32 v28, v72, v28, v68
	v_max_f32_e32 v22, 0, v22
	v_max_f32_e32 v23, 0, v23
	v_add_f32_e32 v24, v24, v60
	v_add_f32_e32 v25, v25, v61
	v_add3_u32 v20, v73, v20, v68
	ds_write_b64 v32, v[30:31]
	ds_write_b64 v28, v[26:27]
	v_max_f32_e32 v24, 0, v24
	v_max_f32_e32 v25, 0, v25
	v_cvt_pk_bf16_f32 v22, v22, v23
	v_cvt_pk_bf16_f32 v23, v24, v25
	ds_write_b64 v32, v[22:23] offset:16384
	ds_write_b64 v20, v[18:19]
	v_or_b32_e32 v18, 48, v66
	s_waitcnt vmcnt(0)
	v_add_f32_e32 v14, v14, v42
	v_add_f32_e32 v15, v15, v43
	v_add_f32_e32 v16, v16, v44
	v_add_f32_e32 v10, v10, v42
	v_add_f32_e32 v11, v11, v43
	v_add_f32_e32 v12, v12, v44
	v_add_f32_e32 v2, v2, v42
	v_add_f32_e32 v3, v3, v43
	v_add_f32_e32 v4, v4, v44
	v_lshrrev_b32_e32 v18, 3, v18
	v_max_f32_e32 v14, 0, v14
	v_max_f32_e32 v15, 0, v15
	v_max_f32_e32 v16, 0, v16
	v_add_f32_e32 v17, v17, v45
	v_max_f32_e32 v10, 0, v10
	v_max_f32_e32 v11, 0, v11
	v_max_f32_e32 v12, 0, v12
	v_add_f32_e32 v13, v13, v45
	v_max_f32_e32 v2, 0, v2
	v_max_f32_e32 v3, 0, v3
	v_max_f32_e32 v4, 0, v4
	v_add_f32_e32 v5, v5, v45
	v_max_f32_e32 v17, 0, v17
	v_cvt_pk_bf16_f32 v14, v14, v15
	v_cvt_pk_bf16_f32 v15, v16, v17
	v_xor_b32_e32 v16, v18, v118
	v_max_f32_e32 v13, 0, v13
	v_cvt_pk_bf16_f32 v10, v10, v11
	v_cvt_pk_bf16_f32 v11, v12, v13
	v_bitop3_b32 v12, v18, v70, 31 bitop3:0x78
	v_max_f32_e32 v5, 0, v5
	v_cvt_pk_bf16_f32 v2, v2, v3
	v_cvt_pk_bf16_f32 v3, v4, v5
	v_bitop3_b32 v4, v18, v71, 31 bitop3:0x78
	v_lshlrev_b32_e32 v16, 4, v16
	v_lshlrev_b32_e32 v12, 4, v12
	v_add_f32_e32 v6, v6, v42
	v_add_f32_e32 v7, v7, v43
	v_lshlrev_b32_e32 v4, 4, v4
	v_add3_u32 v16, v69, v16, v68
	v_add3_u32 v12, v72, v12, v68
	v_max_f32_e32 v6, 0, v6
	v_max_f32_e32 v7, 0, v7
	v_add_f32_e32 v8, v8, v44
	v_add_f32_e32 v9, v9, v45
	v_add3_u32 v4, v73, v4, v68
	ds_write_b64 v16, v[14:15]
	ds_write_b64 v12, v[10:11]
	v_max_f32_e32 v8, 0, v8
	v_max_f32_e32 v9, 0, v9
	v_cvt_pk_bf16_f32 v6, v6, v7
	v_cvt_pk_bf16_f32 v7, v8, v9
	ds_write_b64 v16, v[6:7] offset:16384
	ds_write_b64 v4, v[2:3]
	v_and_b32_e32 v2, 0x1f0, v1
	v_mov_b32_e32 v3, 0
	v_lshl_add_u64 v[2:3], s[0:1], 0, v[2:3]
	s_mov_b64 s[0:1], 0x2000000
	v_ashrrev_i32_e32 v6, 5, v0
	v_lshl_add_u64 v[10:11], v[2:3], 0, s[0:1]
	v_xor_b32_e32 v2, v6, v0
	v_lshlrev_b32_e32 v2, 4, v2
	v_lshlrev_b32_e32 v1, 9, v6
	v_and_b32_e32 v2, 0x1f0, v2
	v_add3_u32 v1, 0, v1, v2
	s_waitcnt lgkmcnt(0)
	s_barrier
	ds_read_b128 v[2:5], v1
	v_ashrrev_i32_e32 v7, 31, v6
	v_add_u32_e32 v1, 0x200, v0
	v_lshlrev_b64 v[6:7], 11, v[6:7]
	v_ashrrev_i32_e32 v14, 5, v1
	v_lshl_add_u64 v[12:13], v[10:11], 0, v[6:7]
	v_xor_b32_e32 v6, v14, v0
	v_lshlrev_b32_e32 v6, 4, v6
	v_lshlrev_b32_e32 v1, 9, v14
	v_and_b32_e32 v6, 0x1f0, v6
	v_add3_u32 v1, 0, v1, v6
	ds_read_b128 v[6:9], v1
	v_ashrrev_i32_e32 v15, 31, v14
	s_waitcnt lgkmcnt(1)
	global_store_dwordx4 v[12:13], v[2:5], off sc1
	v_add_u32_e32 v1, 0x400, v0
	s_nop 0
	v_lshlrev_b64 v[2:3], 11, v[14:15]
	v_lshl_add_u64 v[2:3], v[10:11], 0, v[2:3]
	s_waitcnt lgkmcnt(0)
	global_store_dwordx4 v[2:3], v[6:9], off sc1
	s_nop 1
	v_ashrrev_i32_e32 v6, 5, v1
	v_xor_b32_e32 v2, v6, v0
	v_lshlrev_b32_e32 v2, 4, v2
	v_lshlrev_b32_e32 v1, 9, v6
	v_and_b32_e32 v2, 0x1f0, v2
	v_add3_u32 v1, 0, v1, v2
	ds_read_b128 v[2:5], v1
	v_ashrrev_i32_e32 v7, 31, v6
	v_add_u32_e32 v1, 0x600, v0
	v_lshlrev_b64 v[6:7], 11, v[6:7]
	v_ashrrev_i32_e32 v14, 5, v1
	v_lshl_add_u64 v[12:13], v[10:11], 0, v[6:7]
	v_xor_b32_e32 v6, v14, v0
	v_lshlrev_b32_e32 v6, 4, v6
	v_lshlrev_b32_e32 v1, 9, v14
	v_and_b32_e32 v6, 0x1f0, v6
	v_add3_u32 v1, 0, v1, v6
	ds_read_b128 v[6:9], v1
	v_ashrrev_i32_e32 v15, 31, v14
	s_waitcnt lgkmcnt(1)
	global_store_dwordx4 v[12:13], v[2:5], off sc1
	v_add_u32_e32 v1, 0x800, v0
	s_nop 0
	v_lshlrev_b64 v[2:3], 11, v[14:15]
	v_lshl_add_u64 v[2:3], v[10:11], 0, v[2:3]
	s_waitcnt lgkmcnt(0)
	global_store_dwordx4 v[2:3], v[6:9], off sc1
	s_nop 1
	v_ashrrev_i32_e32 v6, 5, v1
	v_xor_b32_e32 v2, v6, v0
	v_lshlrev_b32_e32 v2, 4, v2
	v_lshlrev_b32_e32 v1, 9, v6
	v_and_b32_e32 v2, 0x1f0, v2
	v_add3_u32 v1, 0, v1, v2
	ds_read_b128 v[2:5], v1
	v_ashrrev_i32_e32 v7, 31, v6
	v_add_u32_e32 v1, 0xa00, v0
	v_lshlrev_b64 v[6:7], 11, v[6:7]
	v_ashrrev_i32_e32 v14, 5, v1
	v_lshl_add_u64 v[12:13], v[10:11], 0, v[6:7]
	v_xor_b32_e32 v6, v14, v0
	v_lshlrev_b32_e32 v6, 4, v6
	v_lshlrev_b32_e32 v1, 9, v14
	v_and_b32_e32 v6, 0x1f0, v6
	v_add3_u32 v1, 0, v1, v6
	ds_read_b128 v[6:9], v1
	v_ashrrev_i32_e32 v15, 31, v14
	s_waitcnt lgkmcnt(1)
	global_store_dwordx4 v[12:13], v[2:5], off sc1
	v_add_u32_e32 v1, 0xc00, v0
	s_nop 0
	v_lshlrev_b64 v[2:3], 11, v[14:15]
	v_lshl_add_u64 v[2:3], v[10:11], 0, v[2:3]
	s_waitcnt lgkmcnt(0)
	global_store_dwordx4 v[2:3], v[6:9], off sc1
	s_nop 1
	v_ashrrev_i32_e32 v6, 5, v1
	v_xor_b32_e32 v2, v6, v0
	v_lshlrev_b32_e32 v2, 4, v2
	v_lshlrev_b32_e32 v1, 9, v6
	v_and_b32_e32 v2, 0x1f0, v2
	v_add3_u32 v1, 0, v1, v2
	ds_read_b128 v[2:5], v1
	v_add_u32_e32 v1, 0xe00, v0
	v_ashrrev_i32_e32 v14, 5, v1
	v_xor_b32_e32 v0, v14, v0
	v_lshlrev_b32_e32 v0, 4, v0
	v_ashrrev_i32_e32 v7, 31, v6
	v_lshlrev_b32_e32 v1, 9, v14
	v_and_b32_e32 v0, 0x1f0, v0
	v_lshlrev_b64 v[6:7], 11, v[6:7]
	v_add3_u32 v0, 0, v1, v0
	v_lshl_add_u64 v[12:13], v[10:11], 0, v[6:7]
	ds_read_b128 v[6:9], v0
	v_ashrrev_i32_e32 v15, 31, v14
	v_lshlrev_b64 v[0:1], 11, v[14:15]
	v_lshl_add_u64 v[0:1], v[10:11], 0, v[0:1]
	s_waitcnt lgkmcnt(1)
	global_store_dwordx4 v[12:13], v[2:5], off sc1
	s_waitcnt lgkmcnt(0)
	global_store_dwordx4 v[0:1], v[6:9], off sc1
	s_endpgm

.LBB2_9:
	s_waitcnt lgkmcnt(0)
	s_nop 1
	v_mfma_f32_32x32x16_bf16 v[80:95], a[192:195], a[128:131], 0
	v_mfma_f32_32x32x16_bf16 v[48:63], a[192:195], a[160:163], 0
	v_mfma_f32_32x32x16_bf16 v[64:79], a[224:227], a[128:131], 0
	v_mfma_f32_32x32x16_bf16 v[32:47], a[224:227], a[160:163], 0
	v_mfma_f32_32x32x16_bf16 v[80:95], a[196:199], a[132:135], v[80:95]
	v_mfma_f32_32x32x16_bf16 v[48:63], a[196:199], a[164:167], v[48:63]
	v_mfma_f32_32x32x16_bf16 v[64:79], a[228:231], a[132:135], v[64:79]
	v_mfma_f32_32x32x16_bf16 v[32:47], a[228:231], a[164:167], v[32:47]
	v_mfma_f32_32x32x16_bf16 v[80:95], a[200:203], a[136:139], v[80:95]
	v_mfma_f32_32x32x16_bf16 v[48:63], a[200:203], a[168:171], v[48:63]
	v_mfma_f32_32x32x16_bf16 v[64:79], a[232:235], a[136:139], v[64:79]
	v_mfma_f32_32x32x16_bf16 v[32:47], a[232:235], a[168:171], v[32:47]
	v_mfma_f32_32x32x16_bf16 v[80:95], a[204:207], a[140:143], v[80:95]
	v_mfma_f32_32x32x16_bf16 v[48:63], a[204:207], a[172:175], v[48:63]
	v_mfma_f32_32x32x16_bf16 v[64:79], a[236:239], a[140:143], v[64:79]
	v_mfma_f32_32x32x16_bf16 v[32:47], a[236:239], a[172:175], v[32:47]
	v_mfma_f32_32x32x16_bf16 v[80:95], a[208:211], a[144:147], v[80:95]
	s_mov_b32 s0, s30
	v_mfma_f32_32x32x16_bf16 v[48:63], a[208:211], a[176:179], v[48:63]
	s_mov_b32 s1, s36
	v_mfma_f32_32x32x16_bf16 v[64:79], a[240:243], a[144:147], v[64:79]
	s_mov_b32 s16, s37
	v_mfma_f32_32x32x16_bf16 v[32:47], a[240:243], a[176:179], v[32:47]
	s_mov_b32 s17, s38
	v_mfma_f32_32x32x16_bf16 v[80:95], a[212:215], a[148:151], v[80:95]
	s_mov_b32 s19, s39
	v_mfma_f32_32x32x16_bf16 v[48:63], a[212:215], a[180:183], v[48:63]
	s_mov_b32 s22, s40
	v_mfma_f32_32x32x16_bf16 v[64:79], a[244:247], a[148:151], v[64:79]
	s_mov_b32 s23, s41
	v_mfma_f32_32x32x16_bf16 v[32:47], a[244:247], a[180:183], v[32:47]
	s_mov_b32 s24, s42
	v_mfma_f32_32x32x16_bf16 v[80:95], a[216:219], a[152:155], v[80:95]
	s_mov_b32 s81, s43
	v_mfma_f32_32x32x16_bf16 v[48:63], a[216:219], a[184:187], v[48:63]
	s_mov_b32 s82, s44
	v_mfma_f32_32x32x16_bf16 v[64:79], a[248:251], a[152:155], v[64:79]
	s_mov_b32 s83, s45
	v_mfma_f32_32x32x16_bf16 v[32:47], a[248:251], a[184:187], v[32:47]
	s_mov_b32 s84, s46
	v_mfma_f32_32x32x16_bf16 v[80:95], a[220:223], a[156:159], v[80:95]
	s_mov_b32 s85, s47
	v_mfma_f32_32x32x16_bf16 v[48:63], a[220:223], a[188:191], v[48:63]
	s_mov_b32 s86, s48
	v_mfma_f32_32x32x16_bf16 v[64:79], a[252:255], a[156:159], v[64:79]
	s_mov_b32 s87, s49
	v_mfma_f32_32x32x16_bf16 v[32:47], a[252:255], a[188:191], v[32:47]
	s_mov_b32 s88, s50
	s_nop 4
	s_waitcnt vmcnt(0) lgkmcnt(0)
	s_barrier
	s_nop 0
	s_mov_b32 m0, s0
	s_nop 0
	buffer_load_dwordx4 v209, s[4:7], s1 offen lds
	s_mov_b32 m0, s16
	s_nop 0
	buffer_load_dwordx4 v210, s[4:7], s17 offen lds
	ds_read_b128 a[192:195], v219 offset:0
	s_mov_b32 m0, s19
	s_nop 0
	buffer_load_dwordx4 v209, s[4:7], s22 offen lds
	ds_read_b128 a[196:199], v220 offset:0
	s_mov_b32 m0, s23
	s_nop 0
	buffer_load_dwordx4 v210, s[4:7], s24 offen lds
	ds_read_b128 a[200:203], v221 offset:0
	s_mov_b32 s22, s6
	s_mov_b32 s23, s7
	s_mov_b32 m0, s81
	s_nop 0
	buffer_load_dwordx4 v211, s[20:23], s82 offen lds
	ds_read_b128 a[204:207], v222 offset:0
	s_mov_b32 m0, s83
	s_nop 0
	buffer_load_dwordx4 v211, s[20:23], s84 offen lds
	ds_read_b128 a[208:211], v219 offset:128
	s_mov_b32 m0, s85
	s_nop 0
	buffer_load_dwordx4 v211, s[20:23], s86 offen lds
	ds_read_b128 a[212:215], v220 offset:128
	s_mov_b32 m0, s87
	s_nop 0
	buffer_load_dwordx4 v211, s[20:23], s88 offen lds
	ds_read_b128 a[216:219], v221 offset:128
	ds_read_b128 a[220:223], v222 offset:128
	v_max3_f32 v96, v80, v81, v64
	v_max3_f32 v97, v82, v83, v65
	v_max3_f32 v96, v96, v66, v67
	ds_read_b128 a[224:227], v219 offset:8192
	v_max3_f32 v96, v96, v84, v85
	v_max3_f32 v97, v97, v86, v87
	v_max3_f32 v96, v96, v68, v69
	v_max3_f32 v97, v97, v70, v71
	ds_read_b128 a[228:231], v220 offset:8192
	v_max3_f32 v96, v96, v88, v89
	v_max3_f32 v97, v97, v90, v91
	v_max3_f32 v96, v96, v72, v73
	v_max3_f32 v97, v97, v74, v75
	ds_read_b128 a[232:235], v221 offset:8192
	v_max3_f32 v96, v96, v92, v93
	v_max3_f32 v97, v97, v94, v95
	v_max3_f32 v96, v96, v76, v77
	v_max3_f32 v97, v97, v78, v79
	ds_read_b128 a[236:239], v222 offset:8192
	v_max3_f32 v98, v48, v49, v32
	v_max3_f32 v99, v50, v51, v33
	v_max3_f32 v98, v98, v34, v35
	ds_read_b128 a[240:243], v219 offset:8320
	v_max3_f32 v98, v98, v52, v53
	v_max3_f32 v99, v99, v54, v55
	v_max3_f32 v98, v98, v36, v37
	v_max3_f32 v99, v99, v38, v39
	ds_read_b128 a[244:247], v220 offset:8320
	v_max3_f32 v98, v98, v56, v57
	v_max3_f32 v99, v99, v58, v59
	v_max3_f32 v98, v98, v40, v41
	v_max3_f32 v99, v99, v42, v43
	ds_read_b128 a[248:251], v221 offset:8320
	v_max3_f32 v98, v98, v60, v61
	v_max3_f32 v99, v99, v62, v63
	v_max3_f32 v98, v98, v44, v45
	v_max3_f32 v99, v99, v46, v47
	ds_read_b128 a[252:255], v222 offset:8320
	v_max_f32_e32 v96, v96, v97
	v_mov_b32_e32 v97, v96
	s_nop 1
	v_permlane32_swap_b32_e32 v96, v97
	v_max_f32_e32 v227, v96, v97
	v_max_f32_e32 v96, v98, v99
	v_mov_b32_e32 v97, v96
	s_nop 1
	v_permlane32_swap_b32_e32 v96, v97
	v_max_f32_e32 v226, v96, v97
	v_sub_f32_e32 v128, v66, v227
	v_mbcnt_lo_u32_b32 v66, -1, 0
	v_mbcnt_hi_u32_b32 v66, -1, v66
	v_sub_f32_e32 v129, v67, v227
	v_xor_b32_e32 v67, 0x80000000, v227
	v_cmp_gt_u32_e32 vcc, 32, v66
	v_sub_f32_e32 v142, v32, v226
	v_mov_b32_e32 v228, 1.0
	v_sub_f32_e32 v143, v33, v226
	v_xor_b32_e32 v33, 0x80000000, v226
	v_cndmask_b32_e64 v66, 0, 1.0, vcc
	s_nop 1
	v_mfma_f32_32x32x2_f32 v[16:31], v66, v67, 0
	v_mbcnt_lo_u32_b32 v32, -1, 0
	v_mbcnt_hi_u32_b32 v32, -1, v32
	v_sub_f32_e32 v80, v80, v227
	v_sub_f32_e32 v81, v81, v227
	v_sub_f32_e32 v82, v82, v227
	v_sub_f32_e32 v83, v83, v227
	v_sub_f32_e32 v84, v84, v227
	v_sub_f32_e32 v85, v85, v227
	v_sub_f32_e32 v86, v86, v227
	v_sub_f32_e32 v87, v87, v227
	v_sub_f32_e32 v88, v88, v227
	v_sub_f32_e32 v89, v89, v227
	v_sub_f32_e32 v90, v90, v227
	v_sub_f32_e32 v91, v91, v227
	v_sub_f32_e32 v92, v92, v227
	v_sub_f32_e32 v93, v93, v227
	v_sub_f32_e32 v94, v94, v227
	v_sub_f32_e32 v95, v95, v227
	v_sub_f32_e32 v64, v64, v227
	v_sub_f32_e32 v65, v65, v227
	v_sub_f32_e32 v130, v68, v227
	s_nop 0
	v_cmp_gt_u32_e32 vcc, 32, v32
	v_sub_f32_e32 v131, v69, v227
	v_sub_f32_e32 v132, v70, v227
	v_sub_f32_e32 v133, v71, v227
	v_sub_f32_e32 v134, v72, v227
	v_sub_f32_e32 v135, v73, v227
	v_sub_f32_e32 v136, v74, v227
	v_sub_f32_e32 v137, v75, v227
	v_sub_f32_e32 v138, v76, v227
	v_sub_f32_e32 v139, v77, v227
	v_sub_f32_e32 v140, v78, v227
	v_sub_f32_e32 v141, v79, v227
	v_sub_f32_e32 v48, v48, v226
	v_sub_f32_e32 v49, v49, v226
	v_sub_f32_e32 v50, v50, v226
	v_sub_f32_e32 v51, v51, v226
	v_sub_f32_e32 v52, v52, v226
	v_sub_f32_e32 v53, v53, v226
	v_sub_f32_e32 v54, v54, v226
	v_sub_f32_e32 v55, v55, v226
	s_nop 1
	v_cndmask_b32_e64 v32, 0, 1.0, vcc
	v_sub_f32_e32 v56, v56, v226
	v_sub_f32_e32 v57, v57, v226
	v_sub_f32_e32 v58, v58, v226
	v_sub_f32_e32 v59, v59, v226
	v_sub_f32_e32 v60, v60, v226
	v_sub_f32_e32 v61, v61, v226
	v_sub_f32_e32 v62, v62, v226
	v_sub_f32_e32 v63, v63, v226
	v_sub_f32_e32 v144, v34, v226
	v_sub_f32_e32 v145, v35, v226
	v_sub_f32_e32 v146, v36, v226
	v_sub_f32_e32 v147, v37, v226
	v_sub_f32_e32 v183, v38, v226
	v_sub_f32_e32 v192, v39, v226
	v_sub_f32_e32 v193, v40, v226
	v_sub_f32_e32 v194, v41, v226
	v_sub_f32_e32 v195, v42, v226
	v_sub_f32_e32 v196, v43, v226
	v_sub_f32_e32 v197, v44, v226
	v_sub_f32_e32 v199, v45, v226
	v_sub_f32_e32 v229, v46, v226
	v_sub_f32_e32 v231, v47, v226
	s_nop 1
	v_mfma_f32_32x32x2_f32 v[0:15], v32, v33, 0
	v_exp_f32_e32 v112, v80
	v_exp_f32_e32 v113, v81
	v_exp_f32_e32 v114, v82
	v_exp_f32_e32 v115, v83
	v_add_f32_e32 v32, v201, v112
	v_add_f32_e32 v33, v201, v113
	v_exp_f32_e32 v116, v84
	v_exp_f32_e32 v117, v85
	v_exp_f32_e32 v118, v86
	v_add_f32_e32 v32, v32, v114
	v_add_f32_e32 v33, v33, v115
	v_exp_f32_e32 v119, v87
	v_exp_f32_e32 v120, v88
	v_add_f32_e32 v32, v32, v116
	v_add_f32_e32 v33, v33, v117
	v_add_f32_e32 v32, v32, v118
	v_exp_f32_e32 v121, v89
	v_exp_f32_e32 v122, v90
	v_exp_f32_e32 v123, v91
	v_add_f32_e32 v33, v33, v119
	v_add_f32_e32 v32, v32, v120
	v_exp_f32_e32 v124, v92
	v_exp_f32_e32 v125, v93
	v_add_f32_e32 v33, v33, v121
	v_add_f32_e32 v32, v32, v122
	v_add_f32_e32 v33, v33, v123
	v_exp_f32_e32 v126, v94
	v_exp_f32_e32 v127, v95
	v_exp_f32_e32 v96, v48
	v_add_f32_e32 v32, v32, v124
	v_add_f32_e32 v33, v33, v125
	v_exp_f32_e32 v97, v49
	v_exp_f32_e32 v98, v50
	v_add_f32_e32 v232, v32, v126
	v_add_f32_e32 v233, v33, v127
	v_add_f32_e32 v32, v201, v96
	v_exp_f32_e32 v99, v51
	v_exp_f32_e32 v100, v52
	v_exp_f32_e32 v101, v53
	v_add_f32_e32 v33, v201, v97
	v_add_f32_e32 v32, v32, v98
	v_exp_f32_e32 v102, v54
	v_exp_f32_e32 v103, v55
	v_add_f32_e32 v33, v33, v99
	v_add_f32_e32 v32, v32, v100
	v_add_f32_e32 v33, v33, v101
	v_exp_f32_e32 v104, v56
	v_exp_f32_e32 v105, v57
	v_exp_f32_e32 v106, v58
	v_add_f32_e32 v32, v32, v102
	v_add_f32_e32 v33, v33, v103
	v_exp_f32_e32 v107, v59
	v_exp_f32_e32 v108, v60
	v_add_f32_e32 v32, v32, v104
	v_add_f32_e32 v33, v33, v105
	v_add_f32_e32 v32, v32, v106
	v_exp_f32_e32 v109, v61
	v_exp_f32_e32 v110, v62
	v_exp_f32_e32 v111, v63
	v_add_f32_e32 v33, v33, v107
	v_add_f32_e32 v32, v32, v108
	s_nop 0
	s_waitcnt lgkmcnt(0)
	v_add_f32_e32 v33, v33, v109
	v_add_f32_e32 v234, v32, v110
	v_add_f32_e32 v235, v33, v111
	v_mfma_f32_32x32x16_bf16 v[80:95], a[192:195], a[128:131], v[16:31]
	ds_read_b64_tr_b16 v[168:169], v208 offset:0
	v_exp_f32_e32 v236, v64
	v_exp_f32_e32 v237, v65
	v_cvt_pk_bf16_f32 v152, v112, v113
	v_exp_f32_e32 v112, v128
	v_exp_f32_e32 v113, v129
	v_mfma_f32_32x32x16_bf16 v[64:79], a[192:195], a[160:163], v[0:15]
	ds_read_b64_tr_b16 v[170:171], v208 offset:0x800
	v_cvt_pk_bf16_f32 v153, v114, v115
	v_exp_f32_e32 v114, v130
	v_exp_f32_e32 v115, v131
	v_mfma_f32_32x32x16_bf16 v[48:63], a[224:227], a[128:131], v[16:31]
	ds_read_b64_tr_b16 v[172:173], v208 offset:0x200
	v_cvt_pk_bf16_f32 v154, v116, v117
	v_mfma_f32_32x32x16_bf16 v[32:47], a[224:227], a[160:163], v[0:15]
	ds_read_b64_tr_b16 v[174:175], v208 offset:0xa00
	ds_read_b64_tr_b16 v[164:165], v208 offset:0x400
	v_exp_f32_e32 v238, v132
	v_exp_f32_e32 v239, v133
	v_cvt_pk_bf16_f32 v155, v118, v119
	v_exp_f32_e32 v184, v134
	v_exp_f32_e32 v185, v135
	v_mfma_f32_32x32x16_bf16 v[80:95], a[196:199], a[132:135], v[80:95]
	ds_read_b64_tr_b16 v[166:167], v208 offset:0xc00
	v_cvt_pk_bf16_f32 v128, v120, v121
	v_exp_f32_e32 v186, v136
	v_exp_f32_e32 v187, v137
	v_mfma_f32_32x32x16_bf16 v[64:79], a[196:199], a[164:167], v[64:79]
	ds_read_b64_tr_b16 v[176:177], v208 offset:0x600
	v_cvt_pk_bf16_f32 v129, v122, v123
	v_exp_f32_e32 v188, v138
	v_exp_f32_e32 v189, v139
	v_mfma_f32_32x32x16_bf16 v[48:63], a[228:231], a[132:135], v[48:63]
	ds_read_b64_tr_b16 v[178:179], v208 offset:0xe00
	v_cvt_pk_bf16_f32 v130, v124, v125
	v_mfma_f32_32x32x16_bf16 v[32:47], a[228:231], a[164:167], v[32:47]
	ds_read_b64_tr_b16 v[160:161], v208 offset:0x1000
	v_exp_f32_e32 v190, v140
	v_exp_f32_e32 v191, v141
	ds_read_b64_tr_b16 v[162:163], v208 offset:0x1800
	v_cvt_pk_bf16_f32 v131, v126, v127
	v_exp_f32_e32 v141, v142
	v_exp_f32_e32 v142, v143
	v_mfma_f32_32x32x16_bf16 v[80:95], a[200:203], a[136:139], v[80:95]
	ds_read_b64_tr_b16 v[156:157], v208 offset:0x1200
	v_cvt_pk_bf16_f32 v180, v96, v97
	v_exp_f32_e32 v143, v144
	v_mfma_f32_32x32x16_bf16 v[64:79], a[200:203], a[168:171], v[64:79]
	ds_read_b64_tr_b16 v[158:159], v208 offset:0x1a00
	v_exp_f32_e32 v240, v145
	v_cvt_pk_bf16_f32 v181, v98, v99
	v_mfma_f32_32x32x16_bf16 v[48:63], a[232:235], a[136:139], v[48:63]
	ds_read_b64_tr_b16 v[148:149], v208 offset:0x1400
	v_exp_f32_e32 v241, v146
	v_exp_f32_e32 v242, v147
	v_cvt_pk_bf16_f32 v182, v100, v101
	v_mfma_f32_32x32x16_bf16 v[32:47], a[232:235], a[168:171], v[32:47]
	ds_read_b64_tr_b16 v[150:151], v208 offset:0x1c00
	ds_read_b64_tr_b16 v[136:137], v208 offset:0x1600
	v_exp_f32_e32 v243, v183
	v_exp_f32_e32 v244, v192
	v_cvt_pk_bf16_f32 v183, v102, v103
	v_exp_f32_e32 v192, v193
	v_exp_f32_e32 v193, v194
	v_mfma_f32_32x32x16_bf16 v[80:95], a[204:207], a[140:143], v[80:95]
	ds_read_b64_tr_b16 v[138:139], v208 offset:0x1e00
	v_cvt_pk_bf16_f32 v144, v104, v105
	v_exp_f32_e32 v194, v195
	v_exp_f32_e32 v195, v196
	v_mfma_f32_32x32x16_bf16 v[64:79], a[204:207], a[172:175], v[64:79]
	ds_read_b64_tr_b16 v[132:133], v208 offset:0x2000
	v_cvt_pk_bf16_f32 v145, v106, v107
	v_exp_f32_e32 v198, v197
	v_exp_f32_e32 v199, v199
	v_mfma_f32_32x32x16_bf16 v[48:63], a[236:239], a[140:143], v[48:63]
	ds_read_b64_tr_b16 v[134:135], v208 offset:0x2800
	v_cvt_pk_bf16_f32 v146, v108, v109
	v_mfma_f32_32x32x16_bf16 v[32:47], a[236:239], a[172:175], v[32:47]
	ds_read_b64_tr_b16 v[124:125], v208 offset:0x2200
	v_exp_f32_e32 v230, v229
	v_exp_f32_e32 v231, v231
	ds_read_b64_tr_b16 v[126:127], v208 offset:0x2a00
	v_cvt_pk_bf16_f32 v147, v110, v111
	s_mov_b32 s0, s51
	v_mfma_f32_32x32x16_bf16 v[80:95], a[208:211], a[144:147], v[80:95]
	ds_read_b64_tr_b16 v[120:121], v208 offset:0x2400
	v_cvt_pk_bf16_f32 v116, v236, v237
	v_add_f32_e32 v96, v232, v236
	v_add_f32_e32 v97, v233, v237
	s_mov_b32 s1, s52
	v_mfma_f32_32x32x16_bf16 v[64:79], a[208:211], a[176:179], v[64:79]
	ds_read_b64_tr_b16 v[122:123], v208 offset:0x2c00
	v_cvt_pk_bf16_f32 v117, v112, v113
	v_add_f32_e32 v96, v96, v112
	v_add_f32_e32 v97, v97, v113
	s_mov_b32 s16, s53
	v_mfma_f32_32x32x16_bf16 v[48:63], a[240:243], a[144:147], v[48:63]
	ds_read_b64_tr_b16 v[112:113], v208 offset:0x2600
	v_cvt_pk_bf16_f32 v118, v114, v115
	v_add_f32_e32 v96, v96, v114
	v_add_f32_e32 v97, v97, v115
	s_mov_b32 s17, s54
	v_mfma_f32_32x32x16_bf16 v[32:47], a[240:243], a[176:179], v[32:47]
	ds_read_b64_tr_b16 v[114:115], v208 offset:0x2e00
	ds_read_b64_tr_b16 v[108:109], v208 offset:0x3000
	v_cvt_pk_bf16_f32 v119, v238, v239
	v_add_f32_e32 v96, v96, v238
	v_add_f32_e32 v97, v97, v239
	s_mov_b32 s19, s55
	v_mfma_f32_32x32x16_bf16 v[80:95], a[212:215], a[148:151], v[80:95]
	ds_read_b64_tr_b16 v[110:111], v208 offset:0x3800
	v_add_f32_e32 v96, v96, v184
	v_add_f32_e32 v97, v97, v185
	s_mov_b32 s24, s56
	v_mfma_f32_32x32x16_bf16 v[64:79], a[212:215], a[180:183], v[64:79]
	ds_read_b64_tr_b16 v[104:105], v208 offset:0x3200
	v_add_f32_e32 v96, v96, v186
	v_add_f32_e32 v97, v97, v187
	s_mov_b32 s81, s57
	v_mfma_f32_32x32x16_bf16 v[48:63], a[244:247], a[148:151], v[48:63]
	ds_read_b64_tr_b16 v[106:107], v208 offset:0x3a00
	v_add_f32_e32 v96, v96, v188
	v_add_f32_e32 v97, v97, v189
	s_mov_b32 s82, s58
	v_mfma_f32_32x32x16_bf16 v[32:47], a[244:247], a[180:183], v[32:47]
	ds_read_b64_tr_b16 v[100:101], v208 offset:0x3400
	ds_read_b64_tr_b16 v[102:103], v208 offset:0x3c00
	v_add_f32_e32 v196, v96, v190
	v_add_f32_e32 v197, v97, v191
	s_mov_b32 s83, s31
	v_mfma_f32_32x32x16_bf16 v[80:95], a[216:219], a[152:155], v[80:95]
	ds_read_b64_tr_b16 v[96:97], v208 offset:0x3600
	v_cvt_pk_bf16_f32 v140, v141, v142
	v_add_f32_e32 v229, v234, v141
	v_add_f32_e32 v142, v235, v142
	s_mov_b32 s84, s36
	v_mfma_f32_32x32x16_bf16 v[64:79], a[216:219], a[184:187], v[64:79]
	ds_read_b64_tr_b16 v[98:99], v208 offset:0x3e00
	v_cvt_pk_bf16_f32 v141, v143, v240
	v_add_f32_e32 v143, v229, v143
	v_add_f32_e32 v229, v142, v240
	v_mfma_f32_32x32x16_bf16 v[48:63], a[248:251], a[152:155], v[48:63]
	s_mov_b32 s85, s59
	v_cvt_pk_bf16_f32 v142, v241, v242
	v_add_f32_e32 v232, v143, v241
	v_add_f32_e32 v229, v229, v242
	v_mfma_f32_32x32x16_bf16 v[32:47], a[248:251], a[184:187], v[32:47]
	s_mov_b32 s86, s60
	v_cvt_pk_bf16_f32 v143, v243, v244
	v_add_f32_e32 v232, v232, v243
	v_add_f32_e32 v229, v229, v244
	v_mfma_f32_32x32x16_bf16 v[80:95], a[220:223], a[156:159], v[80:95]
	s_mov_b32 s87, s61
	v_add_f32_e32 v232, v232, v192
	v_add_f32_e32 v229, v229, v193
	v_mfma_f32_32x32x16_bf16 v[64:79], a[220:223], a[188:191], v[64:79]
	s_mov_b32 s88, s40
	v_add_f32_e32 v232, v232, v194
	v_add_f32_e32 v229, v229, v195
	v_mfma_f32_32x32x16_bf16 v[48:63], a[252:255], a[156:159], v[48:63]
	s_mov_b32 s89, s62
	v_add_f32_e32 v232, v232, v198
	v_add_f32_e32 v229, v229, v199
	v_mfma_f32_32x32x16_bf16 v[32:47], a[252:255], a[188:191], v[32:47]
	s_mov_b32 s90, s63
	v_add_f32_e32 v232, v232, v230
	v_add_f32_e32 v229, v229, v231
	s_nop 4
	v_add_f32_e32 v196, v196, v197
	s_waitcnt vmcnt(0) lgkmcnt(0)
	s_barrier
	s_nop 0
	v_mov_b32_e32 v197, v196
	s_nop 1
	v_permlane32_swap_b32_e32 v196, v197
	v_add_f32_e32 v196, v196, v197
	v_add_f32_e32 v197, v201, v196
	v_add_f32_e32 v196, v232, v229
	v_mov_b32_e32 v229, v196
	s_nop 1
	v_permlane32_swap_b32_e32 v196, v229
	v_add_f32_e32 v196, v196, v229
	v_add_f32_e32 v196, v201, v196
	s_nop 1
	v_mfma_f32_32x32x16_bf16 a[0:15], v[168:171], v[152:155], 0
	s_mov_b32 m0, s0
	s_nop 0
	buffer_load_dwordx4 v209, s[4:7], s1 offen lds
	v_mfma_f32_32x32x16_bf16 a[16:31], v[168:171], v[180:183], 0
	s_mov_b32 m0, s16
	s_nop 0
	buffer_load_dwordx4 v210, s[4:7], s17 offen lds
	ds_read_b128 a[192:195], v204 offset:0
	v_mfma_f32_32x32x16_bf16 a[32:47], v[172:175], v[152:155], 0
	s_mov_b32 m0, s19
	s_nop 0
	buffer_load_dwordx4 v209, s[4:7], s24 offen lds
	ds_read_b128 a[196:199], v205 offset:0
	v_mfma_f32_32x32x16_bf16 a[48:63], v[172:175], v[180:183], 0
	s_mov_b32 m0, s81
	s_nop 0
	buffer_load_dwordx4 v210, s[4:7], s82 offen lds
	ds_read_b128 a[200:203], v206 offset:0
	v_mfma_f32_32x32x16_bf16 a[64:79], v[164:167], v[152:155], 0
	s_mov_b32 m0, s83
	s_nop 0
	buffer_load_dwordx4 v211, s[20:23], s84 offen lds
	ds_read_b128 a[204:207], v207 offset:0
	v_mfma_f32_32x32x16_bf16 a[80:95], v[164:167], v[180:183], 0
	s_mov_b32 m0, s85
	s_nop 0
	buffer_load_dwordx4 v211, s[20:23], s86 offen lds
	ds_read_b128 a[208:211], v204 offset:128
	v_mfma_f32_32x32x16_bf16 a[96:111], v[176:179], v[152:155], 0
	s_mov_b32 m0, s87
	s_nop 0
	buffer_load_dwordx4 v211, s[20:23], s88 offen lds
	ds_read_b128 a[212:215], v205 offset:128
	v_mfma_f32_32x32x16_bf16 a[112:127], v[176:179], v[180:183], 0
	s_mov_b32 m0, s89
	s_nop 0
	buffer_load_dwordx4 v211, s[20:23], s90 offen lds
	ds_read_b128 a[216:219], v206 offset:128
	v_mfma_f32_32x32x16_bf16 a[0:15], v[160:163], v[128:131], a[0:15]
	ds_read_b128 a[220:223], v207 offset:128
	v_max3_f32 v152, v80, v81, v48
	v_max3_f32 v153, v82, v83, v49
	v_max3_f32 v152, v152, v50, v51
	v_mfma_f32_32x32x16_bf16 a[16:31], v[160:163], v[144:147], a[16:31]
	ds_read_b128 a[224:227], v204 offset:8192
	v_max3_f32 v152, v152, v84, v85
	v_max3_f32 v153, v153, v86, v87
	v_max3_f32 v152, v152, v52, v53
	v_max3_f32 v153, v153, v54, v55
	v_mfma_f32_32x32x16_bf16 a[32:47], v[156:159], v[128:131], a[32:47]
	ds_read_b128 a[228:231], v205 offset:8192
	v_max3_f32 v152, v152, v88, v89
	v_max3_f32 v153, v153, v90, v91
	v_max3_f32 v152, v152, v56, v57
	v_max3_f32 v153, v153, v58, v59
	v_mfma_f32_32x32x16_bf16 a[48:63], v[156:159], v[144:147], a[48:63]
	ds_read_b128 a[232:235], v206 offset:8192
	v_max3_f32 v152, v152, v92, v93
	v_max3_f32 v153, v153, v94, v95
	v_max3_f32 v152, v152, v60, v61
	v_max3_f32 v153, v153, v62, v63
	v_mfma_f32_32x32x16_bf16 a[64:79], v[148:151], v[128:131], a[64:79]
	ds_read_b128 a[236:239], v207 offset:8192
	v_max3_f32 v154, v64, v65, v32
	v_max3_f32 v155, v66, v67, v33
	v_max3_f32 v154, v154, v34, v35
	v_mfma_f32_32x32x16_bf16 a[80:95], v[148:151], v[144:147], a[80:95]
	ds_read_b128 a[240:243], v204 offset:8320
	v_max3_f32 v148, v154, v68, v69
	v_max3_f32 v149, v155, v70, v71
	v_max3_f32 v148, v148, v36, v37
	v_max3_f32 v149, v149, v38, v39
	v_mfma_f32_32x32x16_bf16 a[96:111], v[136:139], v[128:131], a[96:111]
	ds_read_b128 a[244:247], v205 offset:8320
	v_max3_f32 v128, v148, v72, v73
	v_max3_f32 v129, v149, v74, v75
	v_max3_f32 v128, v128, v40, v41
	v_max3_f32 v129, v129, v42, v43
	v_mfma_f32_32x32x16_bf16 a[112:127], v[136:139], v[144:147], a[112:127]
	ds_read_b128 a[248:251], v206 offset:8320
	v_max3_f32 v128, v128, v76, v77
	v_max3_f32 v129, v129, v78, v79
	v_max3_f32 v128, v128, v44, v45
	v_max3_f32 v130, v129, v46, v47
	v_mfma_f32_32x32x16_bf16 a[0:15], v[132:135], v[116:119], a[0:15]
	ds_read_b128 a[252:255], v207 offset:8320
	v_max_f32_e32 v129, v152, v153
	v_mov_b32_e32 v131, v129
	s_nop 1
	v_permlane32_swap_b32_e32 v129, v131
	v_max_f32_e32 v129, v129, v131
	v_mfma_f32_32x32x16_bf16 a[16:31], v[132:135], v[140:143], a[16:31]
	v_max_f32_e32 v128, v128, v130
	v_mov_b32_e32 v130, v128
	s_nop 1
	v_permlane32_swap_b32_e32 v128, v130
	v_max_f32_e32 v128, v128, v130
	v_max_f32_e32 v130, v129, v129
	v_max_f32_e32 v131, v128, v128
	v_max_f32_e32 v130, v130, v131
	v_mfma_f32_32x32x16_bf16 a[32:47], v[124:127], v[116:119], a[32:47]
	v_cmp_lt_f32_e32 vcc, s79, v130
	s_cmp_lg_u64 vcc, 0
	s_cselect_b64 s[0:1], -1, 0
	s_cbranch_vccnz .LBB2_58
	v_mov_b32_e32 v229, 1.0

.LBB2_22:
	v_exp_f32_e32 v48, v48
	v_exp_f32_e32 v49, v49
	v_mfma_f32_32x32x16_bf16 v[112:127], a[192:195], a[128:131], v[16:31]
	ds_read_b64_tr_b16 v[180:181], v223 offset:0
	v_cvt_pk_bf16_f32 v164, v128, v129
	v_exp_f32_e32 v50, v50
	v_exp_f32_e32 v51, v51
	v_mfma_f32_32x32x16_bf16 v[96:111], a[192:195], a[160:163], v[0:15]
	ds_read_b64_tr_b16 v[182:183], v223 offset:0x800
	v_cvt_pk_bf16_f32 v165, v130, v131
	v_exp_f32_e32 v230, v52
	v_exp_f32_e32 v231, v53
	v_mfma_f32_32x32x16_bf16 v[80:95], a[224:227], a[128:131], v[16:31]
	ds_read_b64_tr_b16 v[184:185], v223 offset:0x200
	v_cvt_pk_bf16_f32 v166, v132, v133
	v_mfma_f32_32x32x16_bf16 v[64:79], a[224:227], a[160:163], v[0:15]
	ds_read_b64_tr_b16 v[186:187], v223 offset:0xa00
	ds_read_b64_tr_b16 v[176:177], v223 offset:0x400
	v_exp_f32_e32 v242, v54
	v_exp_f32_e32 v243, v55
	v_cvt_pk_bf16_f32 v167, v134, v135
	v_exp_f32_e32 v198, v56
	v_exp_f32_e32 v199, v57
	v_mfma_f32_32x32x16_bf16 v[112:127], a[196:199], a[132:135], v[112:127]
	ds_read_b64_tr_b16 v[178:179], v223 offset:0xc00
	v_cvt_pk_bf16_f32 v128, v136, v137
	v_exp_f32_e32 v232, v58
	v_exp_f32_e32 v233, v59
	v_mfma_f32_32x32x16_bf16 v[96:111], a[196:199], a[164:167], v[96:111]
	ds_read_b64_tr_b16 v[188:189], v223 offset:0x600
	v_cvt_pk_bf16_f32 v129, v138, v139
	v_exp_f32_e32 v234, v60
	v_exp_f32_e32 v235, v61
	v_mfma_f32_32x32x16_bf16 v[80:95], a[228:231], a[132:135], v[80:95]
	ds_read_b64_tr_b16 v[190:191], v223 offset:0xe00
	v_cvt_pk_bf16_f32 v130, v140, v141
	v_mfma_f32_32x32x16_bf16 v[64:79], a[228:231], a[164:167], v[64:79]
	ds_read_b64_tr_b16 v[172:173], v223 offset:0x1000
	v_exp_f32_e32 v236, v62
	v_exp_f32_e32 v237, v63
	ds_read_b64_tr_b16 v[174:175], v223 offset:0x1800
	v_cvt_pk_bf16_f32 v131, v142, v143
	v_exp_f32_e32 v141, v32
	v_exp_f32_e32 v142, v33
	v_mfma_f32_32x32x16_bf16 v[112:127], a[200:203], a[136:139], v[112:127]
	ds_read_b64_tr_b16 v[168:169], v223 offset:0x1200
	v_cvt_pk_bf16_f32 v192, v144, v145
	v_exp_f32_e32 v143, v34
	v_mfma_f32_32x32x16_bf16 v[96:111], a[200:203], a[168:171], v[96:111]
	ds_read_b64_tr_b16 v[170:171], v223 offset:0x1a00
	v_exp_f32_e32 v244, v35
	v_cvt_pk_bf16_f32 v193, v146, v147
	v_mfma_f32_32x32x16_bf16 v[80:95], a[232:235], a[136:139], v[80:95]
	ds_read_b64_tr_b16 v[160:161], v223 offset:0x1400
	v_exp_f32_e32 v245, v36
	v_exp_f32_e32 v246, v37
	v_cvt_pk_bf16_f32 v194, v148, v149
	v_mfma_f32_32x32x16_bf16 v[64:79], a[232:235], a[168:171], v[64:79]
	ds_read_b64_tr_b16 v[162:163], v223 offset:0x1c00
	ds_read_b64_tr_b16 v[136:137], v223 offset:0x1600
	v_exp_f32_e32 v247, v38
	v_exp_f32_e32 v248, v39
	v_cvt_pk_bf16_f32 v195, v150, v151
	v_exp_f32_e32 v148, v40
	v_exp_f32_e32 v149, v41
	v_mfma_f32_32x32x16_bf16 v[112:127], a[204:207], a[140:143], v[112:127]
	ds_read_b64_tr_b16 v[138:139], v223 offset:0x1e00
	v_cvt_pk_bf16_f32 v144, v152, v153
	v_exp_f32_e32 v150, v42
	v_exp_f32_e32 v151, v43
	v_mfma_f32_32x32x16_bf16 v[96:111], a[204:207], a[172:175], v[96:111]
	ds_read_b64_tr_b16 v[132:133], v223 offset:0x2000
	v_cvt_pk_bf16_f32 v145, v154, v155
	v_exp_f32_e32 v152, v44
	v_exp_f32_e32 v153, v45
	v_mfma_f32_32x32x16_bf16 v[80:95], a[236:239], a[140:143], v[80:95]
	ds_read_b64_tr_b16 v[134:135], v223 offset:0x2800
	v_cvt_pk_bf16_f32 v146, v156, v157
	v_mfma_f32_32x32x16_bf16 v[64:79], a[236:239], a[172:175], v[64:79]
	ds_read_b64_tr_b16 v[60:61], v223 offset:0x2200
	v_exp_f32_e32 v154, v46
	v_exp_f32_e32 v155, v47
	ds_read_b64_tr_b16 v[62:63], v223 offset:0x2a00
	v_cvt_pk_bf16_f32 v147, v158, v159
	s_mov_b32 s0, s30
	v_mfma_f32_32x32x16_bf16 v[112:127], a[208:211], a[144:147], v[112:127]
	ds_read_b64_tr_b16 v[56:57], v223 offset:0x2400
	v_cvt_pk_bf16_f32 v52, v48, v49
	v_add_f32_e32 v32, v239, v48
	v_add_f32_e32 v33, v238, v49
	s_mov_b32 s1, s64
	v_mfma_f32_32x32x16_bf16 v[96:111], a[208:211], a[176:179], v[96:111]
	ds_read_b64_tr_b16 v[58:59], v223 offset:0x2c00
	v_cvt_pk_bf16_f32 v53, v50, v51
	v_add_f32_e32 v32, v32, v50
	v_add_f32_e32 v33, v33, v51
	s_mov_b32 s4, s37
	v_mfma_f32_32x32x16_bf16 v[80:95], a[240:243], a[144:147], v[80:95]
	ds_read_b64_tr_b16 v[48:49], v223 offset:0x2600
	v_cvt_pk_bf16_f32 v54, v230, v231
	v_add_f32_e32 v32, v32, v230
	v_add_f32_e32 v33, v33, v231
	s_mov_b32 s5, s65
	v_mfma_f32_32x32x16_bf16 v[64:79], a[240:243], a[176:179], v[64:79]
	ds_read_b64_tr_b16 v[50:51], v223 offset:0x2e00
	ds_read_b64_tr_b16 v[44:45], v223 offset:0x3000
	v_cvt_pk_bf16_f32 v55, v242, v243
	v_add_f32_e32 v32, v32, v242
	v_add_f32_e32 v33, v33, v243
	s_mov_b32 s16, s39
	v_mfma_f32_32x32x16_bf16 v[112:127], a[212:215], a[148:151], v[112:127]
	ds_read_b64_tr_b16 v[46:47], v223 offset:0x3800
	v_add_f32_e32 v32, v32, v198
	v_add_f32_e32 v33, v33, v199
	s_mov_b32 s17, s66
	v_mfma_f32_32x32x16_bf16 v[96:111], a[212:215], a[180:183], v[96:111]
	ds_read_b64_tr_b16 v[40:41], v223 offset:0x3200
	v_add_f32_e32 v32, v32, v232
	v_add_f32_e32 v33, v33, v233
	s_mov_b32 s19, s41
	v_mfma_f32_32x32x16_bf16 v[80:95], a[244:247], a[148:151], v[80:95]
	ds_read_b64_tr_b16 v[42:43], v223 offset:0x3a00
	v_add_f32_e32 v32, v32, v234
	v_add_f32_e32 v33, v33, v235
	s_mov_b32 s22, s67
	v_mfma_f32_32x32x16_bf16 v[64:79], a[244:247], a[180:183], v[64:79]
	ds_read_b64_tr_b16 v[36:37], v223 offset:0x3400
	ds_read_b64_tr_b16 v[38:39], v223 offset:0x3c00
	v_add_f32_e32 v156, v32, v236
	v_add_f32_e32 v157, v33, v237
	s_mov_b32 s24, s43
	v_mfma_f32_32x32x16_bf16 v[112:127], a[216:219], a[152:155], v[112:127]
	ds_read_b64_tr_b16 v[32:33], v223 offset:0x3600
	v_cvt_pk_bf16_f32 v140, v141, v142
	v_add_f32_e32 v158, v240, v141
	v_add_f32_e32 v142, v241, v142
	s_mov_b32 s81, s68
	v_mfma_f32_32x32x16_bf16 v[96:111], a[216:219], a[184:187], v[96:111]
	ds_read_b64_tr_b16 v[34:35], v223 offset:0x3e00
	v_cvt_pk_bf16_f32 v141, v143, v244
	v_add_f32_e32 v143, v158, v143
	v_add_f32_e32 v158, v142, v244
	v_mfma_f32_32x32x16_bf16 v[80:95], a[248:251], a[152:155], v[80:95]
	s_mov_b32 s82, s45
	v_cvt_pk_bf16_f32 v142, v245, v246
	v_add_f32_e32 v159, v143, v245
	v_add_f32_e32 v158, v158, v246
	v_mfma_f32_32x32x16_bf16 v[64:79], a[248:251], a[184:187], v[64:79]
	s_mov_b32 s83, s69
	v_cvt_pk_bf16_f32 v143, v247, v248
	v_add_f32_e32 v159, v159, v247
	v_add_f32_e32 v158, v158, v248
	v_mfma_f32_32x32x16_bf16 v[112:127], a[220:223], a[156:159], v[112:127]
	s_mov_b32 s84, s47
	v_add_f32_e32 v159, v159, v148
	v_add_f32_e32 v158, v158, v149
	v_mfma_f32_32x32x16_bf16 v[96:111], a[220:223], a[188:191], v[96:111]
	s_mov_b32 s85, s70
	v_add_f32_e32 v159, v159, v150
	v_add_f32_e32 v158, v158, v151
	v_mfma_f32_32x32x16_bf16 v[80:95], a[252:255], a[156:159], v[80:95]
	s_mov_b32 s86, s49
	v_add_f32_e32 v159, v159, v152
	v_add_f32_e32 v158, v158, v153
	v_mfma_f32_32x32x16_bf16 v[64:79], a[252:255], a[188:191], v[64:79]
	s_mov_b32 s87, s71
	v_add_f32_e32 v159, v159, v154
	v_add_f32_e32 v158, v158, v155
	s_nop 4
	v_add_f32_e32 v156, v156, v157
	s_waitcnt vmcnt(0) lgkmcnt(0)
	s_barrier
	s_nop 0
	v_mov_b32_e32 v157, v156
	s_nop 1
	v_permlane32_swap_b32_e32 v156, v157
	v_add_f32_e32 v156, v156, v157
	v_add_f32_e32 v231, v197, v156
	v_add_f32_e32 v156, v159, v158
	v_mov_b32_e32 v157, v156
	s_nop 1
	v_permlane32_swap_b32_e32 v156, v157
	v_add_f32_e32 v156, v156, v157
	v_add_f32_e32 v230, v196, v156
	s_nop 1
	v_mfma_f32_32x32x16_bf16 a[0:15], v[180:183], v[164:167], a[0:15]
	v_mfma_f32_32x32x16_bf16 a[16:31], v[180:183], v[192:195], a[16:31]
	ds_read_b128 a[192:195], v219 offset:0
	v_mfma_f32_32x32x16_bf16 a[32:47], v[184:187], v[164:167], a[32:47]
	ds_read_b128 a[196:199], v220 offset:0
	v_mfma_f32_32x32x16_bf16 a[48:63], v[184:187], v[192:195], a[48:63]
	ds_read_b128 a[200:203], v221 offset:0
	v_mfma_f32_32x32x16_bf16 a[64:79], v[176:179], v[164:167], a[64:79]
	s_mov_b32 s22, s6
	s_mov_b32 s23, s7
	s_mov_b32 m0, s24
	s_nop 0
	buffer_load_dwordx4 v211, s[20:23], s81 offen lds
	ds_read_b128 a[204:207], v222 offset:0
	v_mfma_f32_32x32x16_bf16 a[80:95], v[176:179], v[192:195], a[80:95]
	s_mov_b32 m0, s82
	s_nop 0
	buffer_load_dwordx4 v211, s[20:23], s83 offen lds
	ds_read_b128 a[208:211], v219 offset:128
	v_mfma_f32_32x32x16_bf16 a[96:111], v[188:191], v[164:167], a[96:111]
	s_mov_b32 m0, s84
	s_nop 0
	buffer_load_dwordx4 v211, s[20:23], s85 offen lds
	ds_read_b128 a[212:215], v220 offset:128
	v_mfma_f32_32x32x16_bf16 a[112:127], v[188:191], v[192:195], a[112:127]
	s_mov_b32 m0, s86
	s_nop 0
	buffer_load_dwordx4 v211, s[20:23], s87 offen lds
	ds_read_b128 a[216:219], v221 offset:128
	v_mfma_f32_32x32x16_bf16 a[0:15], v[172:175], v[128:131], a[0:15]
	ds_read_b128 a[220:223], v222 offset:128
	v_max3_f32 v156, v112, v113, v80
	v_max3_f32 v157, v114, v115, v81
	v_max3_f32 v156, v156, v82, v83
	v_mfma_f32_32x32x16_bf16 a[16:31], v[172:175], v[144:147], a[16:31]
	ds_read_b128 a[224:227], v219 offset:8192
	v_max3_f32 v156, v156, v116, v117
	v_max3_f32 v157, v157, v118, v119
	v_max3_f32 v156, v156, v84, v85
	v_max3_f32 v157, v157, v86, v87
	v_mfma_f32_32x32x16_bf16 a[32:47], v[168:171], v[128:131], a[32:47]
	ds_read_b128 a[228:231], v220 offset:8192
	v_max3_f32 v156, v156, v120, v121
	v_max3_f32 v157, v157, v122, v123
	v_max3_f32 v156, v156, v88, v89
	v_max3_f32 v157, v157, v90, v91
	v_mfma_f32_32x32x16_bf16 a[48:63], v[168:171], v[144:147], a[48:63]
	ds_read_b128 a[232:235], v221 offset:8192
	v_max3_f32 v156, v156, v124, v125
	v_max3_f32 v157, v157, v126, v127
	v_max3_f32 v156, v156, v92, v93
	v_max3_f32 v157, v157, v94, v95
	v_mfma_f32_32x32x16_bf16 a[64:79], v[160:163], v[128:131], a[64:79]
	ds_read_b128 a[236:239], v222 offset:8192
	v_max3_f32 v158, v96, v97, v64
	v_max3_f32 v159, v98, v99, v65
	v_max3_f32 v158, v158, v66, v67
	v_mfma_f32_32x32x16_bf16 a[80:95], v[160:163], v[144:147], a[80:95]
	ds_read_b128 a[240:243], v219 offset:8320
	v_max3_f32 v158, v158, v100, v101
	v_max3_f32 v159, v159, v102, v103
	v_max3_f32 v158, v158, v68, v69
	v_max3_f32 v159, v159, v70, v71
	v_mfma_f32_32x32x16_bf16 a[96:111], v[136:139], v[128:131], a[96:111]
	ds_read_b128 a[244:247], v220 offset:8320
	v_max3_f32 v128, v158, v104, v105
	v_max3_f32 v129, v159, v106, v107
	v_max3_f32 v128, v128, v72, v73
	v_max3_f32 v129, v129, v74, v75
	v_mfma_f32_32x32x16_bf16 a[112:127], v[136:139], v[144:147], a[112:127]
	ds_read_b128 a[248:251], v221 offset:8320
	v_max3_f32 v128, v128, v108, v109
	v_max3_f32 v129, v129, v110, v111
	v_max3_f32 v128, v128, v76, v77
	v_max3_f32 v130, v129, v78, v79
	v_mfma_f32_32x32x16_bf16 a[0:15], v[132:135], v[52:55], a[0:15]
	ds_read_b128 a[252:255], v222 offset:8320
	v_max_f32_e32 v129, v156, v157
	v_mov_b32_e32 v131, v129
	s_nop 1
	v_permlane32_swap_b32_e32 v129, v131
	v_max_f32_e32 v129, v129, v131
	v_mfma_f32_32x32x16_bf16 a[16:31], v[132:135], v[140:143], a[16:31]
	v_max_f32_e32 v128, v128, v130
	v_mov_b32_e32 v130, v128
	s_nop 1
	v_permlane32_swap_b32_e32 v128, v130
	v_max_f32_e32 v128, v128, v130
	v_max_f32_e32 v130, v129, v129
	v_max_f32_e32 v131, v128, v128
	v_max_f32_e32 v130, v130, v131
	v_mfma_f32_32x32x16_bf16 a[32:47], v[60:63], v[52:55], a[32:47]
	v_cmp_lt_f32_e32 vcc, s79, v130
	s_cmp_lg_u64 vcc, 0
	s_cselect_b64 s[0:1], -1, 0
	s_cbranch_vccnz .LBB2_60
